# K-loop back-edge rotation (docs 7.11): counter/pointer/exit-test and next-iteration scalar setup issued one-per-MFMA inside the iteration's last MFMA block, in 6 GEMM K-loops
# speedup vs baseline: 1.0007x; 1.0007x over previous
; #define PG8_STAGE(bufoff, gbase, voff) do { _Pragma("unroll") for (int _i = 0; _i < 2; ++_i) \
;         __builtin_amdgcn_global_load_lds((const unsigned*)((const char*)(gbase) + (voff)[_i]), (PG8_LAS unsigned*)(lds + (bufoff) + ldsw + _i * 8192), 16, 0, 0); } while (0)
; #define PG8_STAGE_A(bufoff, ptr, h, nx) do { if constexpr (GATHER) { const int ub_ = ((nx) ? gnext : ui) * 256 + (h) * 128; unsigned vv_[2]; _Pragma("unroll") for (int _j = 0; _j < 2; ++_j) vv_[_j] = gofs[ub_ + gL[_j]] + (unsigned)gC[_j]; PG8_STAGE(bufoff, ptr, vv_); } \
;         else { PG8_STAGE(bufoff, (ptr) + (size_t)(h) * hstep, voffA); } } while (0)
; #define PG8_LDA(dst, b, h) do { _Pragma("unroll") for (int m = 0; m < 4; ++m) _Pragma("unroll") for (int k = 0; k < 2; ++k) dst[m][k] = *(const PG8_LAS bf16x8*)(lds + PG8_SA(b, h) + aoff + m * 2048 + k * 1024); } while (0)
; #define PG8_LDB(dst, b, h) do { _Pragma("unroll") for (int n = 0; n < 2; ++n) _Pragma("unroll") for (int k = 0; k < 2; ++k) dst[n][k] = *(const PG8_LAS bf16x8*)(lds + PG8_SB(b, h) + boff + n * 2048 + k * 1024); } while (0)
; #define PG8_WAIT_V(n) asm volatile("s_waitcnt vmcnt(" #n ")" ::: "memory")
; #define PG8_WAIT_L(n) asm volatile("s_waitcnt lgkmcnt(" #n ")" ::: "memory")
; #define PG8_BAR __builtin_amdgcn_s_barrier()
; #define PG8_SCHED __builtin_amdgcn_sched_barrier(0)
; template <class Epi, class Sched, bool ALIGN_EPI = false, bool SP2 = false, bool GATHER = false, bool FP8 = false>
; __device__ __forceinline__ void gemm_phase(PG8_LAS unsigned char* lds, const Gemm g, const Sched& S, const Epi& E, int tid_in  , const PG8_LAS unsigned* gofs = nullptr) {
;     ...
;             PG8_LDB(B0, 0, 0); PG8_LDB(B1, 0, 1); PG8_SCHED; PG8_LDA(At, 0, 0); PG8_STAGE_A(PG8_SA(1, 1), a1, 1, false);
;             PG8_WAIT_V(8); PG8_WAIT_L(0); PG8_BAR; PG8_MMA(0, 0, At, B0); PG8_MMA(0, 1, At, B1); PG8_BAR; PG8_SCHED;
;             PG8_LDA(At, 0, 1); PG8_STAGE(PG8_SB(0, 0), b2, voffB); PG8_STAGE(PG8_SB(0, 1), b2 + hstep, voffB); PG8_STAGE_A(PG8_SA(0, 0), a2, 0, last);
;             PG8_WAIT_V(8); PG8_WAIT_L(0); PG8_BAR; PG8_MMA(1, 0, At, B0); PG8_MMA(1, 1, At, B1); PG8_BAR; PG8_SCHED;
;             PG8_LDB(B0, 1, 0); PG8_LDB(B1, 1, 1); PG8_SCHED; PG8_LDA(At, 1, 0); PG8_STAGE_A(PG8_SA(0, 1), a2, 1, last);
;             PG8_WAIT_V(8); PG8_WAIT_L(0); PG8_BAR; PG8_MMA(0, 0, At, B0); PG8_MMA(0, 1, At, B1); PG8_BAR; PG8_SCHED;
.Lkrot0_body:
	v_add_u32_e32 v4, s59, v189
	v_add_u32_e32 v8, s60, v189
	ds_read_b128 v[28:31], v4
	ds_read_b128 v[32:35], v4 offset:1024
	ds_read_b128 v[20:23], v4 offset:2048
	ds_read_b128 v[24:27], v4 offset:3072
	ds_read_b128 v[12:15], v8
	ds_read_b128 v[16:19], v8 offset:1024
	ds_read_b128 v[4:7], v8 offset:2048
	ds_read_b128 v[8:11], v8 offset:3072
	v_lshl_add_u64 v[184:185], s[26:27], 0, v[170:171]
	s_add_i32 m0, s45, 0xc000
	ds_read_b128 v[176:179], v190
	ds_read_b128 v[180:183], v190 offset:1024
	ds_read_b128 v[218:221], v190 offset:2048
	ds_read_b128 v[222:225], v190 offset:3072
	ds_read_b128 v[226:229], v190 offset:4096
	ds_read_b128 v[230:233], v190 offset:5120
	ds_read_b128 v[234:237], v190 offset:6144
	ds_read_b128 v[238:241], v190 offset:7168
	global_load_lds_dwordx4 v[184:185], off
	v_lshl_add_u64 v[184:185], s[26:27], 0, v[172:173]
	s_add_i32 m0, s45, 0xe000
	s_nop 0
	global_load_lds_dwordx4 v[184:185], off
	s_waitcnt vmcnt(8)
	s_waitcnt lgkmcnt(0)
	s_barrier
	s_setprio 1
	s_waitcnt lgkmcnt(0)
	v_mfma_f32_16x16x128_f8f6f4 v[160:163], v[28:35], v[176:183], v[160:163]
	v_mfma_f32_16x16x128_f8f6f4 v[156:159], v[20:27], v[176:183], v[156:159]
	v_mfma_f32_16x16x128_f8f6f4 v[152:155], v[28:35], v[218:225], v[152:155]
	v_mfma_f32_16x16x128_f8f6f4 v[148:151], v[20:27], v[218:225], v[148:151]
	v_mfma_f32_16x16x128_f8f6f4 v[140:143], v[28:35], v[226:233], v[140:143]
	v_mfma_f32_16x16x128_f8f6f4 v[132:135], v[20:27], v[226:233], v[132:135]
	v_mfma_f32_16x16x128_f8f6f4 v[124:127], v[28:35], v[234:241], v[124:127]
	v_mfma_f32_16x16x128_f8f6f4 v[116:119], v[20:27], v[234:241], v[116:119]
	s_setprio 0
	s_setprio 1
	v_mfma_f32_16x16x128_f8f6f4 v[144:147], v[12:19], v[176:183], v[144:147]
	v_mfma_f32_16x16x128_f8f6f4 v[136:139], v[4:11], v[176:183], v[136:139]
	v_mfma_f32_16x16x128_f8f6f4 v[128:131], v[12:19], v[218:225], v[128:131]
	v_mfma_f32_16x16x128_f8f6f4 v[120:123], v[4:11], v[218:225], v[120:123]
	v_mfma_f32_16x16x128_f8f6f4 v[112:115], v[12:19], v[226:233], v[112:115]
	v_mfma_f32_16x16x128_f8f6f4 v[108:111], v[4:11], v[226:233], v[108:111]
	v_mfma_f32_16x16x128_f8f6f4 v[104:107], v[12:19], v[234:241], v[104:107]
	v_mfma_f32_16x16x128_f8f6f4 v[100:103], v[4:11], v[234:241], v[100:103]
	s_setprio 0
	s_barrier
	s_add_i32 s59, s59, s44
	v_lshl_add_u64 v[176:177], s[34:35], 0, v[164:165]
	s_mov_b32 m0, s59
	ds_read_b128 v[218:221], v190 offset:16384
	ds_read_b128 v[222:225], v190 offset:17408
	ds_read_b128 v[226:229], v190 offset:18432
	ds_read_b128 v[230:233], v190 offset:19456
	ds_read_b128 v[234:237], v190 offset:20480
	ds_read_b128 v[238:241], v190 offset:21504
	ds_read_b128 v[242:245], v190 offset:22528
	ds_read_b128 v[246:249], v190 offset:23552
	global_load_lds_dwordx4 v[176:177], off
	s_add_i32 m0, s59, 0x2000
	v_lshl_add_u64 v[178:179], s[34:35], 0, v[168:169]
	s_add_u32 s34, s34, s10
	s_addc_u32 s35, s35, s11
	s_add_i32 s59, s60, s44
	global_load_lds_dwordx4 v[178:179], off
	v_lshl_add_u64 v[180:181], s[34:35], 0, v[164:165]
	s_mov_b32 m0, s59
	v_lshl_add_u64 v[182:183], s[34:35], 0, v[168:169]
	global_load_lds_dwordx4 v[180:181], off
	s_add_i32 m0, s59, 0x2000
	v_lshl_add_u64 v[184:185], s[28:29], 0, v[0:1]
	global_load_lds_dwordx4 v[182:183], off
	s_mov_b32 m0, s45
	v_lshl_add_u64 v[186:187], s[28:29], 0, v[166:167]
	global_load_lds_dwordx4 v[184:185], off
	s_mov_b32 m0, s46
	s_nop 0
	global_load_lds_dwordx4 v[186:187], off
	s_waitcnt vmcnt(8)
	s_waitcnt lgkmcnt(0)
	s_barrier
	s_setprio 1
	s_waitcnt lgkmcnt(0)
	v_mfma_f32_16x16x128_f8f6f4 v[96:99], v[28:35], v[218:225], v[96:99]
	v_mfma_f32_16x16x128_f8f6f4 v[92:95], v[20:27], v[218:225], v[92:95]
	v_mfma_f32_16x16x128_f8f6f4 v[88:91], v[28:35], v[226:233], v[88:91]
	v_mfma_f32_16x16x128_f8f6f4 v[84:87], v[20:27], v[226:233], v[84:87]
	v_mfma_f32_16x16x128_f8f6f4 v[76:79], v[28:35], v[234:241], v[76:79]
	v_mfma_f32_16x16x128_f8f6f4 v[68:71], v[20:27], v[234:241], v[68:71]
	v_mfma_f32_16x16x128_f8f6f4 v[60:63], v[28:35], v[242:249], v[60:63]
	v_mfma_f32_16x16x128_f8f6f4 v[52:55], v[20:27], v[242:249], v[52:55]
	s_setprio 0
	s_setprio 1
	v_mfma_f32_16x16x128_f8f6f4 v[80:83], v[12:19], v[218:225], v[80:83]
	v_mfma_f32_16x16x128_f8f6f4 v[72:75], v[4:11], v[218:225], v[72:75]
	v_mfma_f32_16x16x128_f8f6f4 v[64:67], v[12:19], v[226:233], v[64:67]
	v_mfma_f32_16x16x128_f8f6f4 v[56:59], v[4:11], v[226:233], v[56:59]
	v_mfma_f32_16x16x128_f8f6f4 v[48:51], v[12:19], v[234:241], v[48:51]
	v_mfma_f32_16x16x128_f8f6f4 v[44:47], v[4:11], v[234:241], v[44:47]
	v_mfma_f32_16x16x128_f8f6f4 v[40:43], v[12:19], v[242:249], v[40:43]
	v_mfma_f32_16x16x128_f8f6f4 v[36:39], v[4:11], v[242:249], v[36:39]
	s_setprio 0
	s_barrier
	s_add_i32 s34, 0, 0x18000
	s_add_i32 s35, 0, 0x1c000
	v_add_u32_e32 v16, s34, v189
	v_add_u32_e32 v32, s35, v189
	ds_read_b128 v[4:7], v16
	ds_read_b128 v[8:11], v16 offset:1024
	ds_read_b128 v[12:15], v16 offset:2048
	ds_read_b128 v[16:19], v16 offset:3072
	ds_read_b128 v[20:23], v32
	ds_read_b128 v[24:27], v32 offset:1024
	ds_read_b128 v[28:31], v32 offset:2048
	ds_read_b128 v[32:35], v32 offset:3072
	s_add_u32 s28, s28, s10
	s_addc_u32 s29, s29, s11
	s_mov_b32 m0, s47
	v_lshl_add_u64 v[192:193], s[28:29], 0, v[0:1]
	ds_read_b128 v[218:221], v190 offset:32768
	ds_read_b128 v[222:225], v190 offset:33792
	ds_read_b128 v[226:229], v190 offset:34816
	ds_read_b128 v[230:233], v190 offset:35840
	ds_read_b128 v[234:237], v190 offset:36864
	ds_read_b128 v[238:241], v190 offset:37888
	ds_read_b128 v[242:245], v190 offset:38912
	ds_read_b128 v[246:249], v190 offset:39936
	global_load_lds_dwordx4 v[192:193], off
	v_lshl_add_u64 v[192:193], s[28:29], 0, v[166:167]
	s_mov_b32 m0, s48
	s_nop 0
	global_load_lds_dwordx4 v[192:193], off
	s_waitcnt vmcnt(8)
	s_waitcnt lgkmcnt(0)
	s_barrier
; #define PG8_STAGE(bufoff, gbase, voff) do { _Pragma("unroll") for (int _i = 0; _i < 2; ++_i) \
;         __builtin_amdgcn_global_load_lds((const unsigned*)((const char*)(gbase) + (voff)[_i]), (PG8_LAS unsigned*)(lds + (bufoff) + ldsw + _i * 8192), 16, 0, 0); } while (0)
; #define PG8_STAGE_A(bufoff, ptr, h, nx) do { if constexpr (GATHER) { const int ub_ = ((nx) ? gnext : ui) * 256 + (h) * 128; unsigned vv_[2]; _Pragma("unroll") for (int _j = 0; _j < 2; ++_j) vv_[_j] = gofs[ub_ + gL[_j]] + (unsigned)gC[_j]; PG8_STAGE(bufoff, ptr, vv_); } \
;         else { PG8_STAGE(bufoff, (ptr) + (size_t)(h) * hstep, voffA); } } while (0)
; #define PG8_LDA(dst, b, h) do { _Pragma("unroll") for (int m = 0; m < 4; ++m) _Pragma("unroll") for (int k = 0; k < 2; ++k) dst[m][k] = *(const PG8_LAS bf16x8*)(lds + PG8_SA(b, h) + aoff + m * 2048 + k * 1024); } while (0)
; #define PG8_WAIT_V(n) asm volatile("s_waitcnt vmcnt(" #n ")" ::: "memory")
; #define PG8_WAIT_L(n) asm volatile("s_waitcnt lgkmcnt(" #n ")" ::: "memory")
; #define PG8_BAR __builtin_amdgcn_s_barrier()
; #define PG8_SCHED __builtin_amdgcn_sched_barrier(0)
; template <class Epi, class Sched, bool ALIGN_EPI = false, bool SP2 = false, bool GATHER = false, bool FP8 = false>
; __device__ __forceinline__ void gemm_phase(PG8_LAS unsigned char* lds, const Gemm g, const Sched& S, const Epi& E, int tid_in  , const PG8_LAS unsigned* gofs = nullptr) {
;     ...
;         for (int t = 0; t < nt; t += 2) {
;             const bool last = (t == nt - 2);
;             const char* a1 = cA + (size_t)(t + 1) * kstep;
;             const char* a2 = last ? nA : cA + (size_t)(t + 2) * kstep; const char* b2 = last ? nB : cB + (size_t)(t + 2) * kstep;
;             const char* a3 = a2 + kstep; const char* b3 = b2 + kstep;
;     ...
;             PG8_LDA(At, 1, 1); PG8_STAGE(PG8_SB(1, 0), b3, voffB); PG8_STAGE(PG8_SB(1, 1), b3 + hstep, voffB); PG8_STAGE_A(PG8_SA(1, 0), a3, 0, last);
;             PG8_WAIT_V(8); PG8_WAIT_L(0); PG8_BAR; PG8_MMA(1, 0, At, B0); PG8_MMA(1, 1, At, B1); PG8_BAR; PG8_SCHED;
	s_setprio 1
	s_waitcnt lgkmcnt(0)
	v_mfma_f32_16x16x128_f8f6f4 v[160:163], v[4:11], v[218:225], v[160:163]
	v_mfma_f32_16x16x128_f8f6f4 v[156:159], v[12:19], v[218:225], v[156:159]
	v_mfma_f32_16x16x128_f8f6f4 v[152:155], v[4:11], v[226:233], v[152:155]
	v_mfma_f32_16x16x128_f8f6f4 v[148:151], v[12:19], v[226:233], v[148:151]
	v_mfma_f32_16x16x128_f8f6f4 v[140:143], v[4:11], v[234:241], v[140:143]
	v_mfma_f32_16x16x128_f8f6f4 v[132:135], v[12:19], v[234:241], v[132:135]
	v_mfma_f32_16x16x128_f8f6f4 v[124:127], v[4:11], v[242:249], v[124:127]
	v_mfma_f32_16x16x128_f8f6f4 v[116:119], v[12:19], v[242:249], v[116:119]
	s_setprio 0
	s_setprio 1
	v_mfma_f32_16x16x128_f8f6f4 v[144:147], v[20:27], v[218:225], v[144:147]
	v_mfma_f32_16x16x128_f8f6f4 v[136:139], v[28:35], v[218:225], v[136:139]
	v_mfma_f32_16x16x128_f8f6f4 v[128:131], v[20:27], v[226:233], v[128:131]
	v_mfma_f32_16x16x128_f8f6f4 v[120:123], v[28:35], v[226:233], v[120:123]
	v_mfma_f32_16x16x128_f8f6f4 v[112:115], v[20:27], v[234:241], v[112:115]
	v_mfma_f32_16x16x128_f8f6f4 v[108:111], v[28:35], v[234:241], v[108:111]
	v_mfma_f32_16x16x128_f8f6f4 v[104:107], v[20:27], v[242:249], v[104:107]
	v_mfma_f32_16x16x128_f8f6f4 v[100:103], v[28:35], v[242:249], v[100:103]
	s_setprio 0
	s_barrier
	s_add_i32 s28, s34, s44
	v_lshl_add_u64 v[176:177], v[176:177], 0, s[38:39]
	s_mov_b32 m0, s28
	ds_read_b128 v[218:221], v190 offset:49152
	ds_read_b128 v[222:225], v190 offset:50176
	ds_read_b128 v[226:229], v190 offset:51200
	ds_read_b128 v[230:233], v190 offset:52224
	ds_read_b128 v[234:237], v190 offset:53248
	ds_read_b128 v[238:241], v190 offset:54272
	ds_read_b128 v[242:245], v190 offset:55296
	ds_read_b128 v[246:249], v190 offset:56320
	global_load_lds_dwordx4 v[176:177], off
	v_lshl_add_u64 v[176:177], v[178:179], 0, s[38:39]
	s_add_i32 m0, s28, 0x2000
	s_add_i32 s28, s35, s44
	global_load_lds_dwordx4 v[176:177], off
	v_lshl_add_u64 v[176:177], v[180:181], 0, s[38:39]
	s_mov_b32 m0, s28
	s_nop 0
	global_load_lds_dwordx4 v[176:177], off
	v_lshl_add_u64 v[176:177], v[182:183], 0, s[38:39]
	s_add_i32 m0, s28, 0x2000
	s_nop 0
	global_load_lds_dwordx4 v[176:177], off
	v_lshl_add_u64 v[176:177], v[184:185], 0, s[38:39]
	s_mov_b32 m0, s49
	s_nop 0
	global_load_lds_dwordx4 v[176:177], off
	v_lshl_add_u64 v[176:177], v[186:187], 0, s[38:39]
	s_mov_b32 m0, s50
	s_nop 0
	global_load_lds_dwordx4 v[176:177], off
	s_waitcnt vmcnt(8)
	s_waitcnt lgkmcnt(0)
	s_barrier
	s_setprio 1
	s_waitcnt lgkmcnt(0)
	v_mfma_f32_16x16x128_f8f6f4 v[96:99], v[4:11], v[218:225], v[96:99]
	s_add_u32 s26, s26, 0x100
	s_addc_u32 s27, s27, 0
	v_mfma_f32_16x16x128_f8f6f4 v[92:95], v[12:19], v[218:225], v[92:95]
	s_add_u32 s56, s56, 0x100
	s_addc_u32 s57, s57, 0
	v_mfma_f32_16x16x128_f8f6f4 v[88:91], v[4:11], v[226:233], v[88:91]
	s_cmp_ge_i32 s58, s51
	s_cselect_b32 vcc_lo, 1, 0
	v_mfma_f32_16x16x128_f8f6f4 v[84:87], v[12:19], v[226:233], v[84:87]
	s_mov_b32 s28, s58
	s_add_i32 s58, s28, 2
	v_mfma_f32_16x16x128_f8f6f4 v[76:79], v[4:11], v[234:241], v[76:79]
	s_add_u32 s34, s26, 0x80
	s_addc_u32 s29, s27, 0
	v_mfma_f32_16x16x128_f8f6f4 v[68:71], v[12:19], v[234:241], v[68:71]
	s_add_i32 s59, 0, 0x10000
	s_cmp_eq_u32 s52, s28
	v_mfma_f32_16x16x128_f8f6f4 v[60:63], v[4:11], v[242:249], v[60:63]
	s_cselect_b32 s29, s5, s29
	s_cselect_b32 s28, s4, s34
	v_mfma_f32_16x16x128_f8f6f4 v[52:55], v[12:19], v[242:249], v[52:55]
	s_cselect_b32 s35, s25, s57
	s_cselect_b32 s34, s24, s56
	s_setprio 0
	s_setprio 1
	v_mfma_f32_16x16x128_f8f6f4 v[80:83], v[20:27], v[218:225], v[80:83]
	s_add_i32 s60, 0, 0x14000
	v_mfma_f32_16x16x128_f8f6f4 v[72:75], v[28:35], v[218:225], v[72:75]
	v_mfma_f32_16x16x128_f8f6f4 v[64:67], v[20:27], v[226:233], v[64:67]
	v_mfma_f32_16x16x128_f8f6f4 v[56:59], v[28:35], v[226:233], v[56:59]
	v_mfma_f32_16x16x128_f8f6f4 v[48:51], v[20:27], v[234:241], v[48:51]
	v_mfma_f32_16x16x128_f8f6f4 v[44:47], v[28:35], v[234:241], v[44:47]
	v_mfma_f32_16x16x128_f8f6f4 v[40:43], v[20:27], v[242:249], v[40:43]
	v_mfma_f32_16x16x128_f8f6f4 v[36:39], v[28:35], v[242:249], v[36:39]
	s_setprio 0
	s_barrier
; #define PG8_STAGE(bufoff, gbase, voff) do { _Pragma("unroll") for (int _i = 0; _i < 2; ++_i) \
;         __builtin_amdgcn_global_load_lds((const unsigned*)((const char*)(gbase) + (voff)[_i]), (PG8_LAS unsigned*)(lds + (bufoff) + ldsw + _i * 8192), 16, 0, 0); } while (0)
; #define PG8_WAIT_V(n) asm volatile("s_waitcnt vmcnt(" #n ")" ::: "memory")
;     __device__ __forceinline__ void operator()(const f32x4 (&acc)[2][2][4][2], const Unit& u, int wr, int wc, int fr, int fq) const {
;     ...
;                 const f32x4 a0 = acc[ai][0][m][0] * inv, a1 = acc[ai][0][m][1] * inv, g0 = acc[ai][1][m][0] * inv, g1 = acc[ai][1][m][1] * inv;
; template <class Epi, class Sched, bool ALIGN_EPI = false, bool SP2 = false, bool GATHER = false, bool FP8 = false>
; __device__ __forceinline__ void gemm_phase(PG8_LAS unsigned char* lds, const Gemm g, const Sched& S, const Epi& E, int tid_in  , const PG8_LAS unsigned* gofs = nullptr) {
;     ...
;         for (int t = 0; t < nt; t += 2) {
;             const bool last = (t == nt - 2);
;             const char* a1 = cA + (size_t)(t + 1) * kstep;
;             const char* a2 = last ? nA : cA + (size_t)(t + 2) * kstep; const char* b2 = last ? nB : cB + (size_t)(t + 2) * kstep;
;             const char* a3 = a2 + kstep; const char* b3 = b2 + kstep;
;             if (last && has_next) S.a_ready(nxt);
;             if constexpr (SP2) {
;             PG8_LDB(B0, 0, 0); PG8_LDB(B1, 0, 1); PG8_SCHED; PG8_LDA(At, 0, 0); PG8_STAGE_A(PG8_SA(1, 1), a1, 1, false);
;             PG8_WAIT_V(8); PG8_WAIT_L(0); PG8_BAR; PG8_MMA(0, 0, At, B0); PG8_MMA(0, 1, At, B1); PG8_BAR; PG8_SCHED;
;             PG8_LDA(At, 0, 1); PG8_STAGE(PG8_SB(0, 0), b2, voffB); PG8_STAGE(PG8_SB(0, 1), b2 + hstep, voffB); PG8_STAGE_A(PG8_SA(0, 0), a2, 0, last);
;             PG8_WAIT_V(8); PG8_WAIT_L(0); PG8_BAR; PG8_MMA(1, 0, At, B0); PG8_MMA(1, 1, At, B1); PG8_BAR; PG8_SCHED;
;             PG8_LDB(B0, 1, 0); PG8_LDB(B1, 1, 1); PG8_SCHED; PG8_LDA(At, 1, 0); PG8_STAGE_A(PG8_SA(0, 1), a2, 1, last);
;             PG8_WAIT_V(8); PG8_WAIT_L(0); PG8_BAR; PG8_MMA(0, 0, At, B0); PG8_MMA(0, 1, At, B1); PG8_BAR; PG8_SCHED;
;             PG8_LDA(At, 1, 1); PG8_STAGE(PG8_SB(1, 0), b3, voffB); PG8_STAGE(PG8_SB(1, 1), b3 + hstep, voffB); PG8_STAGE_A(PG8_SA(1, 0), a3, 0, last);
;             PG8_WAIT_V(8); PG8_WAIT_L(0); PG8_BAR; PG8_MMA(1, 0, At, B0); PG8_MMA(1, 1, At, B1); PG8_BAR; PG8_SCHED;
	s_cmp_eq_u32 vcc_lo, 0
	s_cbranch_scc1 .Lkrot0_body
	s_brev_b32 s26, 28
	v_pk_mul_f32 v[162:163], v[162:163], s[26:27] op_sel_hi:[1,0]
	v_pk_mul_f32 v[160:161], v[160:161], s[26:27] op_sel_hi:[1,0]
	v_pk_mul_f32 v[158:159], v[158:159], s[26:27] op_sel_hi:[1,0]
	v_pk_mul_f32 v[156:157], v[156:157], s[26:27] op_sel_hi:[1,0]
	v_pk_mul_f32 v[180:181], v[146:147], s[26:27] op_sel_hi:[1,0]
	v_pk_mul_f32 v[182:183], v[144:145], s[26:27] op_sel_hi:[1,0]
	v_pk_mul_f32 v[176:177], v[138:139], s[26:27] op_sel_hi:[1,0]
	v_pk_mul_f32 v[178:179], v[136:137], s[26:27] op_sel_hi:[1,0]
	v_pk_mul_f32 v[144:145], v[154:155], s[26:27] op_sel_hi:[1,0]
	v_pk_mul_f32 v[146:147], v[152:153], s[26:27] op_sel_hi:[1,0]
	v_pk_mul_f32 v[136:137], v[150:151], s[26:27] op_sel_hi:[1,0]
	v_pk_mul_f32 v[138:139], v[148:149], s[26:27] op_sel_hi:[1,0]
	v_pk_mul_f32 v[152:153], v[130:131], s[26:27] op_sel_hi:[1,0]
	v_pk_mul_f32 v[154:155], v[128:129], s[26:27] op_sel_hi:[1,0]
	v_pk_mul_f32 v[148:149], v[122:123], s[26:27] op_sel_hi:[1,0]
	v_pk_mul_f32 v[150:151], v[120:121], s[26:27] op_sel_hi:[1,0]
	v_pk_mul_f32 v[128:129], v[142:143], s[26:27] op_sel_hi:[1,0]
	v_pk_mul_f32 v[130:131], v[140:141], s[26:27] op_sel_hi:[1,0]
	v_pk_mul_f32 v[120:121], v[134:135], s[26:27] op_sel_hi:[1,0]
	v_pk_mul_f32 v[122:123], v[132:133], s[26:27] op_sel_hi:[1,0]
	v_pk_mul_f32 v[140:141], v[114:115], s[26:27] op_sel_hi:[1,0]
	v_pk_mul_f32 v[142:143], v[112:113], s[26:27] op_sel_hi:[1,0]
	v_pk_mul_f32 v[132:133], v[110:111], s[26:27] op_sel_hi:[1,0]
	v_pk_mul_f32 v[134:135], v[108:109], s[26:27] op_sel_hi:[1,0]
	v_pk_mul_f32 v[112:113], v[126:127], s[26:27] op_sel_hi:[1,0]
	v_pk_mul_f32 v[114:115], v[124:125], s[26:27] op_sel_hi:[1,0]
	v_pk_mul_f32 v[108:109], v[118:119], s[26:27] op_sel_hi:[1,0]
	v_pk_mul_f32 v[110:111], v[116:117], s[26:27] op_sel_hi:[1,0]
	v_pk_mul_f32 v[106:107], v[106:107], s[26:27] op_sel_hi:[1,0]
	v_pk_mul_f32 v[116:117], v[104:105], s[26:27] op_sel_hi:[1,0]
	v_pk_mul_f32 v[102:103], v[102:103], s[26:27] op_sel_hi:[1,0]
	v_pk_mul_f32 v[100:101], v[100:101], s[26:27] op_sel_hi:[1,0]
	v_pk_mul_f32 v[98:99], v[98:99], s[26:27] op_sel_hi:[1,0]
	v_pk_mul_f32 v[96:97], v[96:97], s[26:27] op_sel_hi:[1,0]
	v_pk_mul_f32 v[94:95], v[94:95], s[26:27] op_sel_hi:[1,0]
	v_pk_mul_f32 v[92:93], v[92:93], s[26:27] op_sel_hi:[1,0]
	v_pk_mul_f32 v[82:83], v[82:83], s[26:27] op_sel_hi:[1,0]
	v_pk_mul_f32 v[104:105], v[80:81], s[26:27] op_sel_hi:[1,0]
	v_pk_mul_f32 v[74:75], v[74:75], s[26:27] op_sel_hi:[1,0]
	v_pk_mul_f32 v[80:81], v[72:73], s[26:27] op_sel_hi:[1,0]
	v_pk_mul_f32 v[34:35], v[90:91], s[26:27] op_sel_hi:[1,0]
	v_pk_mul_f32 v[72:73], v[88:89], s[26:27] op_sel_hi:[1,0]
	v_pk_mul_f32 v[28:29], v[86:87], s[26:27] op_sel_hi:[1,0]
	v_pk_mul_f32 v[32:33], v[84:85], s[26:27] op_sel_hi:[1,0]
	v_pk_mul_f32 v[66:67], v[66:67], s[26:27] op_sel_hi:[1,0]
	v_pk_mul_f32 v[64:65], v[64:65], s[26:27] op_sel_hi:[1,0]
	v_pk_mul_f32 v[58:59], v[58:59], s[26:27] op_sel_hi:[1,0]
	v_pk_mul_f32 v[56:57], v[56:57], s[26:27] op_sel_hi:[1,0]
	v_pk_mul_f32 v[18:19], v[78:79], s[26:27] op_sel_hi:[1,0]
	v_pk_mul_f32 v[24:25], v[76:77], s[26:27] op_sel_hi:[1,0]
	v_pk_mul_f32 v[12:13], v[70:71], s[26:27] op_sel_hi:[1,0]
	v_pk_mul_f32 v[16:17], v[68:69], s[26:27] op_sel_hi:[1,0]
	v_pk_mul_f32 v[50:51], v[50:51], s[26:27] op_sel_hi:[1,0]
	v_pk_mul_f32 v[48:49], v[48:49], s[26:27] op_sel_hi:[1,0]
	v_pk_mul_f32 v[30:31], v[46:47], s[26:27] op_sel_hi:[1,0]
	v_pk_mul_f32 v[44:45], v[44:45], s[26:27] op_sel_hi:[1,0]
	v_pk_mul_f32 v[8:9], v[62:63], s[26:27] op_sel_hi:[1,0]
	v_pk_mul_f32 v[10:11], v[60:61], s[26:27] op_sel_hi:[1,0]
	v_pk_mul_f32 v[4:5], v[54:55], s[26:27] op_sel_hi:[1,0]
	v_pk_mul_f32 v[6:7], v[52:53], s[26:27] op_sel_hi:[1,0]
	v_pk_mul_f32 v[22:23], v[42:43], s[26:27] op_sel_hi:[1,0]
	v_pk_mul_f32 v[26:27], v[40:41], s[26:27] op_sel_hi:[1,0]
	v_pk_mul_f32 v[14:15], v[38:39], s[26:27] op_sel_hi:[1,0]
	v_pk_mul_f32 v[20:21], v[36:37], s[26:27] op_sel_hi:[1,0]

; #define PG8_STAGE(bufoff, gbase, voff) do { _Pragma("unroll") for (int _i = 0; _i < 2; ++_i) \
;         __builtin_amdgcn_global_load_lds((const unsigned*)((const char*)(gbase) + (voff)[_i]), (PG8_LAS unsigned*)(lds + (bufoff) + ldsw + _i * 8192), 16, 0, 0); } while (0)
; #define PG8_STAGE_A(bufoff, ptr, h, nx) do { if constexpr (GATHER) { const int ub_ = ((nx) ? gnext : ui) * 256 + (h) * 128; unsigned vv_[2]; _Pragma("unroll") for (int _j = 0; _j < 2; ++_j) vv_[_j] = gofs[ub_ + gL[_j]] + (unsigned)gC[_j]; PG8_STAGE(bufoff, ptr, vv_); } \
;         else { PG8_STAGE(bufoff, (ptr) + (size_t)(h) * hstep, voffA); } } while (0)
; #define PG8_LDA(dst, b, h) do { _Pragma("unroll") for (int m = 0; m < 4; ++m) _Pragma("unroll") for (int k = 0; k < 2; ++k) dst[m][k] = *(const PG8_LAS bf16x8*)(lds + PG8_SA(b, h) + aoff + m * 2048 + k * 1024); } while (0)
; #define PG8_LDB(dst, b, h) do { _Pragma("unroll") for (int n = 0; n < 2; ++n) _Pragma("unroll") for (int k = 0; k < 2; ++k) dst[n][k] = *(const PG8_LAS bf16x8*)(lds + PG8_SB(b, h) + boff + n * 2048 + k * 1024); } while (0)
; #define PG8_WAIT_V(n) asm volatile("s_waitcnt vmcnt(" #n ")" ::: "memory")
; #define PG8_WAIT_L(n) asm volatile("s_waitcnt lgkmcnt(" #n ")" ::: "memory")
; #define PG8_BAR __builtin_amdgcn_s_barrier()
; #define PG8_SCHED __builtin_amdgcn_sched_barrier(0)
; template <class Epi, class Sched, bool ALIGN_EPI = false, bool SP2 = false, bool GATHER = false, bool FP8 = false>
; __device__ __forceinline__ void gemm_phase(PG8_LAS unsigned char* lds, const Gemm g, const Sched& S, const Epi& E, int tid_in  , const PG8_LAS unsigned* gofs = nullptr) {
;     ...
;             PG8_LDB(B0, 0, 0); PG8_LDB(B1, 0, 1); PG8_SCHED; PG8_LDA(At, 0, 0); PG8_STAGE_A(PG8_SA(1, 1), a1, 1, false);
;             PG8_WAIT_V(8); PG8_WAIT_L(0); PG8_BAR; PG8_MMA(0, 0, At, B0); PG8_MMA(0, 1, At, B1); PG8_BAR; PG8_SCHED;
;             PG8_LDA(At, 0, 1); PG8_STAGE(PG8_SB(0, 0), b2, voffB); PG8_STAGE(PG8_SB(0, 1), b2 + hstep, voffB); PG8_STAGE_A(PG8_SA(0, 0), a2, 0, last);
;             PG8_WAIT_V(8); PG8_WAIT_L(0); PG8_BAR; PG8_MMA(1, 0, At, B0); PG8_MMA(1, 1, At, B1); PG8_BAR; PG8_SCHED;
.Lkrot1_body:
	v_add_u32_e32 v144, s68, v195
	v_add_u32_e32 v163, s69, v195
	ds_read_b128 v[132:135], v144
	ds_read_b128 v[136:139], v144 offset:1024
	ds_read_b128 v[140:143], v144 offset:2048
	ds_read_b128 v[144:147], v144 offset:3072
	ds_read_b128 v[164:167], v163
	ds_read_b128 v[168:171], v163 offset:1024
	ds_read_b128 v[176:179], v163 offset:2048
	ds_read_b128 v[180:183], v163 offset:3072
	v_lshl_add_u64 v[172:173], s[34:35], 0, v[158:159]
	s_add_i32 m0, s51, 0xc000
	ds_read_b128 v[184:187], v197
	ds_read_b128 v[188:191], v197 offset:1024
	ds_read_b128 v[218:221], v197 offset:2048
	ds_read_b128 v[222:225], v197 offset:3072
	ds_read_b128 v[226:229], v197 offset:4096
	ds_read_b128 v[230:233], v197 offset:5120
	ds_read_b128 v[234:237], v197 offset:6144
	ds_read_b128 v[238:241], v197 offset:7168
	global_load_lds_dwordx4 v[172:173], off
	v_lshl_add_u64 v[172:173], s[34:35], 0, v[160:161]
	s_add_i32 m0, s51, 0xe000
	s_nop 0
	global_load_lds_dwordx4 v[172:173], off
	s_waitcnt vmcnt(8)
	s_waitcnt lgkmcnt(0)
	s_barrier
	s_setprio 1
	s_waitcnt lgkmcnt(0)
	v_mfma_f32_16x16x32_bf16 v[124:127], v[132:135], v[184:187], v[124:127]
	v_mfma_f32_16x16x32_bf16 v[116:119], v[140:143], v[184:187], v[116:119]
	v_mfma_f32_16x16x32_bf16 v[108:111], v[132:135], v[218:221], v[108:111]
	v_mfma_f32_16x16x32_bf16 v[100:103], v[140:143], v[218:221], v[100:103]
	v_mfma_f32_16x16x32_bf16 v[92:95], v[132:135], v[226:229], v[92:95]
	v_mfma_f32_16x16x32_bf16 v[84:87], v[140:143], v[226:229], v[84:87]
	v_mfma_f32_16x16x32_bf16 v[76:79], v[132:135], v[234:237], v[76:79]
	v_mfma_f32_16x16x32_bf16 v[68:71], v[140:143], v[234:237], v[68:71]
	v_mfma_f32_16x16x32_bf16 v[124:127], v[136:139], v[188:191], v[124:127]
	v_mfma_f32_16x16x32_bf16 v[116:119], v[144:147], v[188:191], v[116:119]
	v_mfma_f32_16x16x32_bf16 v[108:111], v[136:139], v[222:225], v[108:111]
	v_mfma_f32_16x16x32_bf16 v[100:103], v[144:147], v[222:225], v[100:103]
	v_mfma_f32_16x16x32_bf16 v[92:95], v[136:139], v[230:233], v[92:95]
	v_mfma_f32_16x16x32_bf16 v[84:87], v[144:147], v[230:233], v[84:87]
	v_mfma_f32_16x16x32_bf16 v[76:79], v[136:139], v[238:241], v[76:79]
	v_mfma_f32_16x16x32_bf16 v[68:71], v[144:147], v[238:241], v[68:71]
	s_setprio 0
	s_setprio 1
	v_mfma_f32_16x16x32_bf16 v[128:131], v[164:167], v[184:187], v[128:131]
	v_mfma_f32_16x16x32_bf16 v[120:123], v[176:179], v[184:187], v[120:123]
	v_mfma_f32_16x16x32_bf16 v[112:115], v[164:167], v[218:221], v[112:115]
	v_mfma_f32_16x16x32_bf16 v[104:107], v[176:179], v[218:221], v[104:107]
	v_mfma_f32_16x16x32_bf16 v[96:99], v[164:167], v[226:229], v[96:99]
	v_mfma_f32_16x16x32_bf16 v[88:91], v[176:179], v[226:229], v[88:91]
	v_mfma_f32_16x16x32_bf16 v[80:83], v[164:167], v[234:237], v[80:83]
	v_mfma_f32_16x16x32_bf16 v[72:75], v[176:179], v[234:237], v[72:75]
	v_mfma_f32_16x16x32_bf16 v[128:131], v[168:171], v[188:191], v[128:131]
	v_mfma_f32_16x16x32_bf16 v[120:123], v[180:183], v[188:191], v[120:123]
	v_mfma_f32_16x16x32_bf16 v[112:115], v[168:171], v[222:225], v[112:115]
	v_mfma_f32_16x16x32_bf16 v[104:107], v[180:183], v[222:225], v[104:107]
	v_mfma_f32_16x16x32_bf16 v[96:99], v[168:171], v[230:233], v[96:99]
	v_mfma_f32_16x16x32_bf16 v[88:91], v[180:183], v[230:233], v[88:91]
	v_mfma_f32_16x16x32_bf16 v[80:83], v[168:171], v[238:241], v[80:83]
	v_mfma_f32_16x16x32_bf16 v[72:75], v[180:183], v[238:241], v[72:75]
	s_setprio 0
	s_barrier
	s_add_i32 s68, s68, s43
	v_lshl_add_u64 v[172:173], s[66:67], 0, v[150:151]
	s_mov_b32 m0, s68
	ds_read_b128 v[184:187], v197 offset:16384
	ds_read_b128 v[188:191], v197 offset:17408
	ds_read_b128 v[218:221], v197 offset:18432
	ds_read_b128 v[222:225], v197 offset:19456
	ds_read_b128 v[226:229], v197 offset:20480
	ds_read_b128 v[230:233], v197 offset:21504
	ds_read_b128 v[234:237], v197 offset:22528
	ds_read_b128 v[238:241], v197 offset:23552
	global_load_lds_dwordx4 v[172:173], off
	s_add_i32 m0, s68, 0x2000
	v_lshl_add_u64 v[192:193], s[66:67], 0, v[0:1]
	s_add_u32 s66, s66, s14
	s_addc_u32 s67, s67, s15
	s_add_i32 s68, s69, s43
	global_load_lds_dwordx4 v[192:193], off
	v_lshl_add_u64 v[198:199], s[66:67], 0, v[150:151]
	s_mov_b32 m0, s68
	v_lshl_add_u64 v[200:201], s[66:67], 0, v[0:1]
	global_load_lds_dwordx4 v[198:199], off
	s_add_i32 m0, s68, 0x2000
	v_lshl_add_u64 v[204:205], s[36:37], 0, v[152:153]
	global_load_lds_dwordx4 v[200:201], off
	s_mov_b32 m0, s51
	v_lshl_add_u64 v[208:209], s[36:37], 0, v[148:149]
	global_load_lds_dwordx4 v[204:205], off
	s_mov_b32 m0, s52
	s_nop 0
	global_load_lds_dwordx4 v[208:209], off
	s_waitcnt vmcnt(8)
	s_waitcnt lgkmcnt(0)
	s_barrier
; #define PG8_STAGE_A(bufoff, ptr, h, nx) do { if constexpr (GATHER) { const int ub_ = ((nx) ? gnext : ui) * 256 + (h) * 128; unsigned vv_[2]; _Pragma("unroll") for (int _j = 0; _j < 2; ++_j) vv_[_j] = gofs[ub_ + gL[_j]] + (unsigned)gC[_j]; PG8_STAGE(bufoff, ptr, vv_); } \
;         else { PG8_STAGE(bufoff, (ptr) + (size_t)(h) * hstep, voffA); } } while (0)
; #define PG8_LDA(dst, b, h) do { _Pragma("unroll") for (int m = 0; m < 4; ++m) _Pragma("unroll") for (int k = 0; k < 2; ++k) dst[m][k] = *(const PG8_LAS bf16x8*)(lds + PG8_SA(b, h) + aoff + m * 2048 + k * 1024); } while (0)
; #define PG8_LDB(dst, b, h) do { _Pragma("unroll") for (int n = 0; n < 2; ++n) _Pragma("unroll") for (int k = 0; k < 2; ++k) dst[n][k] = *(const PG8_LAS bf16x8*)(lds + PG8_SB(b, h) + boff + n * 2048 + k * 1024); } while (0)
; #define PG8_WAIT_V(n) asm volatile("s_waitcnt vmcnt(" #n ")" ::: "memory")
; #define PG8_WAIT_L(n) asm volatile("s_waitcnt lgkmcnt(" #n ")" ::: "memory")
; #define PG8_BAR __builtin_amdgcn_s_barrier()
; #define PG8_SCHED __builtin_amdgcn_sched_barrier(0)
; template <class Epi, class Sched, bool ALIGN_EPI = false, bool SP2 = false, bool GATHER = false, bool FP8 = false>
; __device__ __forceinline__ void gemm_phase(PG8_LAS unsigned char* lds, const Gemm g, const Sched& S, const Epi& E, int tid_in  , const PG8_LAS unsigned* gofs = nullptr) {
;     ...
;             PG8_WAIT_V(8); PG8_WAIT_L(0); PG8_BAR; PG8_MMA(1, 0, At, B0); PG8_MMA(1, 1, At, B1); PG8_BAR; PG8_SCHED;
;             PG8_LDB(B0, 1, 0); PG8_LDB(B1, 1, 1); PG8_SCHED; PG8_LDA(At, 1, 0); PG8_STAGE_A(PG8_SA(0, 1), a2, 1, last);
;             PG8_WAIT_V(8); PG8_WAIT_L(0); PG8_BAR; PG8_MMA(0, 0, At, B0); PG8_MMA(0, 1, At, B1); PG8_BAR; PG8_SCHED;
	s_setprio 1
	s_waitcnt lgkmcnt(0)
	v_mfma_f32_16x16x32_bf16 v[60:63], v[132:135], v[184:187], v[60:63]
	v_mfma_f32_16x16x32_bf16 v[52:55], v[140:143], v[184:187], v[52:55]
	v_mfma_f32_16x16x32_bf16 v[44:47], v[132:135], v[218:221], v[44:47]
	v_mfma_f32_16x16x32_bf16 v[36:39], v[140:143], v[218:221], v[36:39]
	v_mfma_f32_16x16x32_bf16 v[28:31], v[132:135], v[226:229], v[28:31]
	v_mfma_f32_16x16x32_bf16 v[20:23], v[140:143], v[226:229], v[20:23]
	v_mfma_f32_16x16x32_bf16 v[12:15], v[132:135], v[234:237], v[12:15]
	v_mfma_f32_16x16x32_bf16 v[4:7], v[140:143], v[234:237], v[4:7]
	v_mfma_f32_16x16x32_bf16 v[60:63], v[136:139], v[188:191], v[60:63]
	v_mfma_f32_16x16x32_bf16 v[52:55], v[144:147], v[188:191], v[52:55]
	v_mfma_f32_16x16x32_bf16 v[44:47], v[136:139], v[222:225], v[44:47]
	v_mfma_f32_16x16x32_bf16 v[36:39], v[144:147], v[222:225], v[36:39]
	v_mfma_f32_16x16x32_bf16 v[28:31], v[136:139], v[230:233], v[28:31]
	v_mfma_f32_16x16x32_bf16 v[20:23], v[144:147], v[230:233], v[20:23]
	v_mfma_f32_16x16x32_bf16 v[12:15], v[136:139], v[238:241], v[12:15]
	v_mfma_f32_16x16x32_bf16 v[4:7], v[144:147], v[238:241], v[4:7]
	s_setprio 0
	s_setprio 1
	v_mfma_f32_16x16x32_bf16 v[64:67], v[164:167], v[184:187], v[64:67]
	v_mfma_f32_16x16x32_bf16 v[56:59], v[176:179], v[184:187], v[56:59]
	v_mfma_f32_16x16x32_bf16 v[48:51], v[164:167], v[218:221], v[48:51]
	v_mfma_f32_16x16x32_bf16 v[40:43], v[176:179], v[218:221], v[40:43]
	v_mfma_f32_16x16x32_bf16 v[32:35], v[164:167], v[226:229], v[32:35]
	v_mfma_f32_16x16x32_bf16 v[24:27], v[176:179], v[226:229], v[24:27]
	v_mfma_f32_16x16x32_bf16 v[16:19], v[164:167], v[234:237], v[16:19]
	v_mfma_f32_16x16x32_bf16 v[8:11], v[176:179], v[234:237], v[8:11]
	v_mfma_f32_16x16x32_bf16 v[64:67], v[168:171], v[188:191], v[64:67]
	v_mfma_f32_16x16x32_bf16 v[56:59], v[180:183], v[188:191], v[56:59]
	v_mfma_f32_16x16x32_bf16 v[48:51], v[168:171], v[222:225], v[48:51]
	v_mfma_f32_16x16x32_bf16 v[40:43], v[180:183], v[222:225], v[40:43]
	v_mfma_f32_16x16x32_bf16 v[32:35], v[168:171], v[230:233], v[32:35]
	v_mfma_f32_16x16x32_bf16 v[24:27], v[180:183], v[230:233], v[24:27]
	v_mfma_f32_16x16x32_bf16 v[16:19], v[168:171], v[238:241], v[16:19]
	v_mfma_f32_16x16x32_bf16 v[8:11], v[180:183], v[238:241], v[8:11]
	s_setprio 0
	s_barrier
	s_add_i32 s66, 0, 0x18000
	s_add_i32 s67, 0, 0x1c000
	v_add_u32_e32 v144, s66, v195
	v_add_u32_e32 v163, s67, v195
	ds_read_b128 v[132:135], v144
	ds_read_b128 v[136:139], v144 offset:1024
	ds_read_b128 v[140:143], v144 offset:2048
	ds_read_b128 v[144:147], v144 offset:3072
	ds_read_b128 v[164:167], v163
	ds_read_b128 v[168:171], v163 offset:1024
	ds_read_b128 v[176:179], v163 offset:2048
	ds_read_b128 v[180:183], v163 offset:3072
	s_add_u32 s36, s36, s14
	s_addc_u32 s37, s37, s15
	s_mov_b32 m0, s53
	v_lshl_add_u64 v[242:243], s[36:37], 0, v[152:153]
	ds_read_b128 v[184:187], v197 offset:32768
	ds_read_b128 v[188:191], v197 offset:33792
	ds_read_b128 v[218:221], v197 offset:34816
	ds_read_b128 v[222:225], v197 offset:35840
	ds_read_b128 v[226:229], v197 offset:36864
	ds_read_b128 v[230:233], v197 offset:37888
	ds_read_b128 v[234:237], v197 offset:38912
	ds_read_b128 v[238:241], v197 offset:39936
	global_load_lds_dwordx4 v[242:243], off
	v_lshl_add_u64 v[242:243], s[36:37], 0, v[148:149]
	s_mov_b32 m0, s54
	s_nop 0
	global_load_lds_dwordx4 v[242:243], off
	s_waitcnt vmcnt(8)
	s_waitcnt lgkmcnt(0)
	s_barrier
	s_setprio 1
	s_waitcnt lgkmcnt(0)
	v_mfma_f32_16x16x32_bf16 v[124:127], v[132:135], v[184:187], v[124:127]
	v_mfma_f32_16x16x32_bf16 v[116:119], v[140:143], v[184:187], v[116:119]
	v_mfma_f32_16x16x32_bf16 v[108:111], v[132:135], v[218:221], v[108:111]
	v_mfma_f32_16x16x32_bf16 v[100:103], v[140:143], v[218:221], v[100:103]
	v_mfma_f32_16x16x32_bf16 v[92:95], v[132:135], v[226:229], v[92:95]
	v_mfma_f32_16x16x32_bf16 v[84:87], v[140:143], v[226:229], v[84:87]
	v_mfma_f32_16x16x32_bf16 v[76:79], v[132:135], v[234:237], v[76:79]
	v_mfma_f32_16x16x32_bf16 v[68:71], v[140:143], v[234:237], v[68:71]
	v_mfma_f32_16x16x32_bf16 v[124:127], v[136:139], v[188:191], v[124:127]
	v_mfma_f32_16x16x32_bf16 v[116:119], v[144:147], v[188:191], v[116:119]
	v_mfma_f32_16x16x32_bf16 v[108:111], v[136:139], v[222:225], v[108:111]
	v_mfma_f32_16x16x32_bf16 v[100:103], v[144:147], v[222:225], v[100:103]
	v_mfma_f32_16x16x32_bf16 v[92:95], v[136:139], v[230:233], v[92:95]
	v_mfma_f32_16x16x32_bf16 v[84:87], v[144:147], v[230:233], v[84:87]
	v_mfma_f32_16x16x32_bf16 v[76:79], v[136:139], v[238:241], v[76:79]
	v_mfma_f32_16x16x32_bf16 v[68:71], v[144:147], v[238:241], v[68:71]
	s_setprio 0
	s_setprio 1
	v_mfma_f32_16x16x32_bf16 v[128:131], v[164:167], v[184:187], v[128:131]
	v_mfma_f32_16x16x32_bf16 v[120:123], v[176:179], v[184:187], v[120:123]
	v_mfma_f32_16x16x32_bf16 v[112:115], v[164:167], v[218:221], v[112:115]
	v_mfma_f32_16x16x32_bf16 v[104:107], v[176:179], v[218:221], v[104:107]
	v_mfma_f32_16x16x32_bf16 v[96:99], v[164:167], v[226:229], v[96:99]
	v_mfma_f32_16x16x32_bf16 v[88:91], v[176:179], v[226:229], v[88:91]
	v_mfma_f32_16x16x32_bf16 v[80:83], v[164:167], v[234:237], v[80:83]
	v_mfma_f32_16x16x32_bf16 v[72:75], v[176:179], v[234:237], v[72:75]
	v_mfma_f32_16x16x32_bf16 v[128:131], v[168:171], v[188:191], v[128:131]
	v_mfma_f32_16x16x32_bf16 v[120:123], v[180:183], v[188:191], v[120:123]
	v_mfma_f32_16x16x32_bf16 v[112:115], v[168:171], v[222:225], v[112:115]
	v_mfma_f32_16x16x32_bf16 v[104:107], v[180:183], v[222:225], v[104:107]
	v_mfma_f32_16x16x32_bf16 v[96:99], v[168:171], v[230:233], v[96:99]
	v_mfma_f32_16x16x32_bf16 v[88:91], v[180:183], v[230:233], v[88:91]
	v_mfma_f32_16x16x32_bf16 v[80:83], v[168:171], v[238:241], v[80:83]
	v_mfma_f32_16x16x32_bf16 v[72:75], v[180:183], v[238:241], v[72:75]
	s_setprio 0
	s_barrier
; #define PG8_STAGE(bufoff, gbase, voff) do { _Pragma("unroll") for (int _i = 0; _i < 2; ++_i) \
;         __builtin_amdgcn_global_load_lds((const unsigned*)((const char*)(gbase) + (voff)[_i]), (PG8_LAS unsigned*)(lds + (bufoff) + ldsw + _i * 8192), 16, 0, 0); } while (0)
; #define PG8_STAGE_A(bufoff, ptr, h, nx) do { if constexpr (GATHER) { const int ub_ = ((nx) ? gnext : ui) * 256 + (h) * 128; unsigned vv_[2]; _Pragma("unroll") for (int _j = 0; _j < 2; ++_j) vv_[_j] = gofs[ub_ + gL[_j]] + (unsigned)gC[_j]; PG8_STAGE(bufoff, ptr, vv_); } \
;         else { PG8_STAGE(bufoff, (ptr) + (size_t)(h) * hstep, voffA); } } while (0)
; #define PG8_LDA(dst, b, h) do { _Pragma("unroll") for (int m = 0; m < 4; ++m) _Pragma("unroll") for (int k = 0; k < 2; ++k) dst[m][k] = *(const PG8_LAS bf16x8*)(lds + PG8_SA(b, h) + aoff + m * 2048 + k * 1024); } while (0)
; #define PG8_WAIT_V(n) asm volatile("s_waitcnt vmcnt(" #n ")" ::: "memory")
; #define PG8_WAIT_L(n) asm volatile("s_waitcnt lgkmcnt(" #n ")" ::: "memory")
; #define PG8_BAR __builtin_amdgcn_s_barrier()
; #define PG8_SCHED __builtin_amdgcn_sched_barrier(0)
; template <class Epi, class Sched, bool ALIGN_EPI = false, bool SP2 = false, bool GATHER = false, bool FP8 = false>
; __device__ __forceinline__ void gemm_phase(PG8_LAS unsigned char* lds, const Gemm g, const Sched& S, const Epi& E, int tid_in  , const PG8_LAS unsigned* gofs = nullptr) {
;     ...
;         for (int t = 0; t < nt; t += 2) {
;             const bool last = (t == nt - 2);
;             const char* a1 = cA + (size_t)(t + 1) * kstep;
;             const char* a2 = last ? nA : cA + (size_t)(t + 2) * kstep; const char* b2 = last ? nB : cB + (size_t)(t + 2) * kstep;
;             const char* a3 = a2 + kstep; const char* b3 = b2 + kstep;
;     ...
;             PG8_LDA(At, 1, 1); PG8_STAGE(PG8_SB(1, 0), b3, voffB); PG8_STAGE(PG8_SB(1, 1), b3 + hstep, voffB); PG8_STAGE_A(PG8_SA(1, 0), a3, 0, last);
;             PG8_WAIT_V(8); PG8_WAIT_L(0); PG8_BAR; PG8_MMA(1, 0, At, B0); PG8_MMA(1, 1, At, B1); PG8_BAR; PG8_SCHED;
	s_add_i32 s36, s66, s43
	v_lshl_add_u64 v[172:173], v[172:173], 0, s[38:39]
	s_mov_b32 m0, s36
	ds_read_b128 v[184:187], v197 offset:49152
	ds_read_b128 v[188:191], v197 offset:50176
	ds_read_b128 v[218:221], v197 offset:51200
	ds_read_b128 v[222:225], v197 offset:52224
	ds_read_b128 v[226:229], v197 offset:53248
	ds_read_b128 v[230:233], v197 offset:54272
	ds_read_b128 v[234:237], v197 offset:55296
	ds_read_b128 v[238:241], v197 offset:56320
	global_load_lds_dwordx4 v[172:173], off
	v_lshl_add_u64 v[172:173], v[192:193], 0, s[38:39]
	s_add_i32 m0, s36, 0x2000
	s_add_i32 s36, s67, s43
	global_load_lds_dwordx4 v[172:173], off
	v_lshl_add_u64 v[172:173], v[198:199], 0, s[38:39]
	s_mov_b32 m0, s36
	s_nop 0
	global_load_lds_dwordx4 v[172:173], off
	v_lshl_add_u64 v[172:173], v[200:201], 0, s[38:39]
	s_add_i32 m0, s36, 0x2000
	s_nop 0
	global_load_lds_dwordx4 v[172:173], off
	v_lshl_add_u64 v[172:173], v[204:205], 0, s[38:39]
	s_mov_b32 m0, s57
	s_nop 0
	global_load_lds_dwordx4 v[172:173], off
	v_lshl_add_u64 v[172:173], v[208:209], 0, s[38:39]
	s_mov_b32 m0, s58
	s_nop 0
	global_load_lds_dwordx4 v[172:173], off
	s_waitcnt vmcnt(8)
	s_waitcnt lgkmcnt(0)
	s_barrier
	s_setprio 1
	s_waitcnt lgkmcnt(0)
	v_mfma_f32_16x16x32_bf16 v[60:63], v[132:135], v[184:187], v[60:63]
	s_add_u32 s34, s34, 0x100
	v_mfma_f32_16x16x32_bf16 v[52:55], v[140:143], v[184:187], v[52:55]
	s_addc_u32 s35, s35, 0
	v_mfma_f32_16x16x32_bf16 v[44:47], v[132:135], v[218:221], v[44:47]
	s_add_u32 s63, s63, 0x100
	v_mfma_f32_16x16x32_bf16 v[36:39], v[140:143], v[218:221], v[36:39]
	s_addc_u32 s64, s64, 0
	v_mfma_f32_16x16x32_bf16 v[28:31], v[132:135], v[226:229], v[28:31]
	s_cmp_ge_i32 s65, s55
	v_mfma_f32_16x16x32_bf16 v[20:23], v[140:143], v[226:229], v[20:23]
	s_cselect_b32 vcc_lo, 1, 0
	v_mfma_f32_16x16x32_bf16 v[12:15], v[132:135], v[234:237], v[12:15]
	s_mov_b32 s36, s65
	v_mfma_f32_16x16x32_bf16 v[4:7], v[140:143], v[234:237], v[4:7]
	s_add_i32 s65, s36, 2
	v_mfma_f32_16x16x32_bf16 v[60:63], v[136:139], v[188:191], v[60:63]
	s_add_u32 s66, s34, 0x80
	v_mfma_f32_16x16x32_bf16 v[52:55], v[144:147], v[188:191], v[52:55]
	s_addc_u32 s37, s35, 0
	v_mfma_f32_16x16x32_bf16 v[44:47], v[136:139], v[222:225], v[44:47]
	s_add_i32 s68, 0, 0x10000
	v_mfma_f32_16x16x32_bf16 v[36:39], v[144:147], v[222:225], v[36:39]
	s_cmp_eq_u32 s59, s36
	v_mfma_f32_16x16x32_bf16 v[28:31], v[136:139], v[230:233], v[28:31]
	s_cselect_b32 s37, s5, s37
	v_mfma_f32_16x16x32_bf16 v[20:23], v[144:147], v[230:233], v[20:23]
	s_cselect_b32 s36, s4, s66
	v_mfma_f32_16x16x32_bf16 v[12:15], v[136:139], v[238:241], v[12:15]
	s_cselect_b32 s67, s29, s64
	v_mfma_f32_16x16x32_bf16 v[4:7], v[144:147], v[238:241], v[4:7]
	s_cselect_b32 s66, s28, s63
	s_setprio 0
	s_setprio 1
	v_mfma_f32_16x16x32_bf16 v[64:67], v[164:167], v[184:187], v[64:67]
	s_add_i32 s69, 0, 0x14000
	v_mfma_f32_16x16x32_bf16 v[56:59], v[176:179], v[184:187], v[56:59]
	v_mfma_f32_16x16x32_bf16 v[48:51], v[164:167], v[218:221], v[48:51]
	v_mfma_f32_16x16x32_bf16 v[40:43], v[176:179], v[218:221], v[40:43]
	v_mfma_f32_16x16x32_bf16 v[32:35], v[164:167], v[226:229], v[32:35]
	v_mfma_f32_16x16x32_bf16 v[24:27], v[176:179], v[226:229], v[24:27]
	v_mfma_f32_16x16x32_bf16 v[16:19], v[164:167], v[234:237], v[16:19]
	v_mfma_f32_16x16x32_bf16 v[8:11], v[176:179], v[234:237], v[8:11]
	v_mfma_f32_16x16x32_bf16 v[64:67], v[168:171], v[188:191], v[64:67]
	v_mfma_f32_16x16x32_bf16 v[56:59], v[180:183], v[188:191], v[56:59]
	v_mfma_f32_16x16x32_bf16 v[48:51], v[168:171], v[222:225], v[48:51]
	v_mfma_f32_16x16x32_bf16 v[40:43], v[180:183], v[222:225], v[40:43]
	v_mfma_f32_16x16x32_bf16 v[32:35], v[168:171], v[230:233], v[32:35]
	v_mfma_f32_16x16x32_bf16 v[24:27], v[180:183], v[230:233], v[24:27]
	v_mfma_f32_16x16x32_bf16 v[16:19], v[168:171], v[238:241], v[16:19]
	v_mfma_f32_16x16x32_bf16 v[8:11], v[180:183], v[238:241], v[8:11]
	s_setprio 0
	s_barrier
	s_cmp_eq_u32 vcc_lo, 0
	s_cbranch_scc1 .Lkrot1_body

; #define PG8_STAGE(bufoff, gbase, voff) do { _Pragma("unroll") for (int _i = 0; _i < 2; ++_i) \
;         __builtin_amdgcn_global_load_lds((const unsigned*)((const char*)(gbase) + (voff)[_i]), (PG8_LAS unsigned*)(lds + (bufoff) + ldsw + _i * 8192), 16, 0, 0); } while (0)
; #define PG8_STAGE_A(bufoff, ptr, h, nx) do { if constexpr (GATHER) { const int ub_ = ((nx) ? gnext : ui) * 256 + (h) * 128; unsigned vv_[2]; _Pragma("unroll") for (int _j = 0; _j < 2; ++_j) vv_[_j] = gofs[ub_ + gL[_j]] + (unsigned)gC[_j]; PG8_STAGE(bufoff, ptr, vv_); } \
;         else { PG8_STAGE(bufoff, (ptr) + (size_t)(h) * hstep, voffA); } } while (0)
; #define PG8_LDA(dst, b, h) do { _Pragma("unroll") for (int m = 0; m < 4; ++m) _Pragma("unroll") for (int k = 0; k < 2; ++k) dst[m][k] = *(const PG8_LAS bf16x8*)(lds + PG8_SA(b, h) + aoff + m * 2048 + k * 1024); } while (0)
; #define PG8_LDB(dst, b, h) do { _Pragma("unroll") for (int n = 0; n < 2; ++n) _Pragma("unroll") for (int k = 0; k < 2; ++k) dst[n][k] = *(const PG8_LAS bf16x8*)(lds + PG8_SB(b, h) + boff + n * 2048 + k * 1024); } while (0)
; #define PG8_WAIT_V(n) asm volatile("s_waitcnt vmcnt(" #n ")" ::: "memory")
; template <class Epi, class Sched, bool ALIGN_EPI = false, bool SP2 = false, bool GATHER = false, bool FP8 = false>
; __device__ __forceinline__ void gemm_phase(PG8_LAS unsigned char* lds, const Gemm g, const Sched& S, const Epi& E, int tid_in  , const PG8_LAS unsigned* gofs = nullptr) {
;     ...
;             const bool last = (t == nt - 2);
;             const char* a1 = cA + (size_t)(t + 1) * kstep;
;             const char* a2 = last ? nA : cA + (size_t)(t + 2) * kstep; const char* b2 = last ? nB : cB + (size_t)(t + 2) * kstep;
;             const char* a3 = a2 + kstep; const char* b3 = b2 + kstep;
;             if (last && has_next) S.a_ready(nxt);
;             if constexpr (SP2) {
;             PG8_LDB(B0, 0, 0); PG8_LDB(B1, 0, 1); PG8_SCHED; PG8_LDA(At, 0, 0); PG8_STAGE_A(PG8_SA(1, 1), a1, 1, false);
;             PG8_WAIT_V(8); PG8_WAIT_L(0); PG8_BAR; PG8_MMA(0, 0, At, B0); PG8_MMA(0, 1, At, B1); PG8_BAR; PG8_SCHED;
;             PG8_LDA(At, 0, 1); PG8_STAGE(PG8_SB(0, 0), b2, voffB); PG8_STAGE(PG8_SB(0, 1), b2 + hstep, voffB); PG8_STAGE_A(PG8_SA(0, 0), a2, 0, last);
;             PG8_WAIT_V(8); PG8_WAIT_L(0); PG8_BAR; PG8_MMA(1, 0, At, B0); PG8_MMA(1, 1, At, B1); PG8_BAR; PG8_SCHED;
.LBB0_657:
	s_add_i32 s46, s20, 2
	s_add_u32 s47, s18, 0x80
	s_addc_u32 s21, s19, 0
	s_add_i32 s50, 0, 0x10000
	s_cmp_eq_u32 s40, s20
	s_cselect_b32 s21, s5, s21
	s_cselect_b32 s20, s4, s47
	s_cselect_b32 s49, s17, s45
	s_cselect_b32 s48, s16, s44
	s_add_i32 s47, 0, 0x14000
.Lkrot2_body:
	v_add_u32_e32 v153, s50, v150
	ds_read_b128 v[142:145], v153
	ds_read_b128 v[146:149], v153 offset:1024
	ds_read_b128 v[154:157], v153 offset:2048
	ds_read_b128 v[158:161], v153 offset:3072
	v_add_u32_e32 v153, s47, v150
	ds_read_b128 v[162:165], v153
	ds_read_b128 v[166:169], v153 offset:1024
	ds_read_b128 v[170:173], v153 offset:2048
	ds_read_b128 v[174:177], v153 offset:3072
	v_lshl_add_u64 v[208:209], s[18:19], 0, v[138:139]
	s_add_i32 m0, s26, 0xc000
	ds_read_b128 v[178:181], v152
	ds_read_b128 v[182:185], v152 offset:1024
	ds_read_b128 v[186:189], v152 offset:2048
	ds_read_b128 v[190:193], v152 offset:3072
	ds_read_b128 v[194:197], v152 offset:4096
	ds_read_b128 v[198:201], v152 offset:5120
	ds_read_b128 v[202:205], v152 offset:6144
	ds_read_b128 v[218:221], v152 offset:7168
	global_load_lds_dwordx4 v[208:209], off
	v_lshl_add_u64 v[208:209], s[18:19], 0, v[140:141]
	s_add_i32 m0, s26, 0xe000
	s_nop 0
	global_load_lds_dwordx4 v[208:209], off
	s_waitcnt vmcnt(8)
	s_waitcnt lgkmcnt(0)
	s_barrier
	s_setprio 1
	s_waitcnt lgkmcnt(0)
	v_mfma_f32_16x16x32_bf16 v[128:131], v[142:145], v[178:181], v[128:131]
	v_mfma_f32_16x16x32_bf16 v[124:127], v[154:157], v[178:181], v[124:127]
	v_mfma_f32_16x16x32_bf16 v[120:123], v[142:145], v[186:189], v[120:123]
	v_mfma_f32_16x16x32_bf16 v[116:119], v[154:157], v[186:189], v[116:119]
	v_mfma_f32_16x16x32_bf16 v[108:111], v[142:145], v[194:197], v[108:111]
	v_mfma_f32_16x16x32_bf16 v[100:103], v[154:157], v[194:197], v[100:103]
	v_mfma_f32_16x16x32_bf16 v[92:95], v[142:145], v[202:205], v[92:95]
	v_mfma_f32_16x16x32_bf16 v[84:87], v[154:157], v[202:205], v[84:87]
	v_mfma_f32_16x16x32_bf16 v[128:131], v[146:149], v[182:185], v[128:131]
	v_mfma_f32_16x16x32_bf16 v[124:127], v[158:161], v[182:185], v[124:127]
	v_mfma_f32_16x16x32_bf16 v[120:123], v[146:149], v[190:193], v[120:123]
	v_mfma_f32_16x16x32_bf16 v[116:119], v[158:161], v[190:193], v[116:119]
	v_mfma_f32_16x16x32_bf16 v[108:111], v[146:149], v[198:201], v[108:111]
	v_mfma_f32_16x16x32_bf16 v[100:103], v[158:161], v[198:201], v[100:103]
	v_mfma_f32_16x16x32_bf16 v[92:95], v[146:149], v[218:221], v[92:95]
	v_mfma_f32_16x16x32_bf16 v[84:87], v[158:161], v[218:221], v[84:87]
	s_setprio 0
	s_setprio 1
	v_mfma_f32_16x16x32_bf16 v[112:115], v[162:165], v[178:181], v[112:115]
	v_mfma_f32_16x16x32_bf16 v[104:107], v[170:173], v[178:181], v[104:107]
	v_mfma_f32_16x16x32_bf16 v[96:99], v[162:165], v[186:189], v[96:99]
	v_mfma_f32_16x16x32_bf16 v[88:91], v[170:173], v[186:189], v[88:91]
	v_mfma_f32_16x16x32_bf16 v[80:83], v[162:165], v[194:197], v[80:83]
	v_mfma_f32_16x16x32_bf16 v[76:79], v[170:173], v[194:197], v[76:79]
	v_mfma_f32_16x16x32_bf16 v[72:75], v[162:165], v[202:205], v[72:75]
	v_mfma_f32_16x16x32_bf16 v[68:71], v[170:173], v[202:205], v[68:71]
	v_mfma_f32_16x16x32_bf16 v[112:115], v[166:169], v[182:185], v[112:115]
	v_mfma_f32_16x16x32_bf16 v[104:107], v[174:177], v[182:185], v[104:107]
	v_mfma_f32_16x16x32_bf16 v[96:99], v[166:169], v[190:193], v[96:99]
	v_mfma_f32_16x16x32_bf16 v[88:91], v[174:177], v[190:193], v[88:91]
	v_mfma_f32_16x16x32_bf16 v[80:83], v[166:169], v[198:201], v[80:83]
	v_mfma_f32_16x16x32_bf16 v[76:79], v[174:177], v[198:201], v[76:79]
	v_mfma_f32_16x16x32_bf16 v[72:75], v[166:169], v[218:221], v[72:75]
	v_mfma_f32_16x16x32_bf16 v[68:71], v[174:177], v[218:221], v[68:71]
	s_setprio 0
	s_barrier
	s_add_i32 s50, s50, s24
	v_lshl_add_u64 v[208:209], s[48:49], 0, v[134:135]
	s_mov_b32 m0, s50
	ds_read_b128 v[178:181], v152 offset:16384
	ds_read_b128 v[182:185], v152 offset:17408
	ds_read_b128 v[186:189], v152 offset:18432
	ds_read_b128 v[190:193], v152 offset:19456
	ds_read_b128 v[194:197], v152 offset:20480
	ds_read_b128 v[198:201], v152 offset:21504
	ds_read_b128 v[202:205], v152 offset:22528
	ds_read_b128 v[218:221], v152 offset:23552
	global_load_lds_dwordx4 v[208:209], off
	s_add_i32 m0, s50, 0x2000
	v_lshl_add_u64 v[222:223], s[48:49], 0, v[0:1]
	s_add_u32 s48, s48, s0
	s_addc_u32 s49, s49, s1
	s_add_i32 s47, s47, s24
	global_load_lds_dwordx4 v[222:223], off
	v_lshl_add_u64 v[224:225], s[48:49], 0, v[134:135]
	s_mov_b32 m0, s47
	v_lshl_add_u64 v[226:227], s[48:49], 0, v[0:1]
	global_load_lds_dwordx4 v[224:225], off
	s_add_i32 m0, s47, 0x2000
	v_lshl_add_u64 v[228:229], s[20:21], 0, v[136:137]
	global_load_lds_dwordx4 v[226:227], off
	s_mov_b32 m0, s26
	v_lshl_add_u64 v[230:231], s[20:21], 0, v[132:133]
	global_load_lds_dwordx4 v[228:229], off
	s_mov_b32 m0, s27
	s_nop 0
	global_load_lds_dwordx4 v[230:231], off
	s_waitcnt vmcnt(8)
	s_waitcnt lgkmcnt(0)
	s_barrier
; #define PG8_STAGE_A(bufoff, ptr, h, nx) do { if constexpr (GATHER) { const int ub_ = ((nx) ? gnext : ui) * 256 + (h) * 128; unsigned vv_[2]; _Pragma("unroll") for (int _j = 0; _j < 2; ++_j) vv_[_j] = gofs[ub_ + gL[_j]] + (unsigned)gC[_j]; PG8_STAGE(bufoff, ptr, vv_); } \
;         else { PG8_STAGE(bufoff, (ptr) + (size_t)(h) * hstep, voffA); } } while (0)
; #define PG8_LDA(dst, b, h) do { _Pragma("unroll") for (int m = 0; m < 4; ++m) _Pragma("unroll") for (int k = 0; k < 2; ++k) dst[m][k] = *(const PG8_LAS bf16x8*)(lds + PG8_SA(b, h) + aoff + m * 2048 + k * 1024); } while (0)
; #define PG8_LDB(dst, b, h) do { _Pragma("unroll") for (int n = 0; n < 2; ++n) _Pragma("unroll") for (int k = 0; k < 2; ++k) dst[n][k] = *(const PG8_LAS bf16x8*)(lds + PG8_SB(b, h) + boff + n * 2048 + k * 1024); } while (0)
; #define PG8_WAIT_V(n) asm volatile("s_waitcnt vmcnt(" #n ")" ::: "memory")
; #define PG8_WAIT_L(n) asm volatile("s_waitcnt lgkmcnt(" #n ")" ::: "memory")
; #define PG8_BAR __builtin_amdgcn_s_barrier()
; #define PG8_SCHED __builtin_amdgcn_sched_barrier(0)
; template <class Epi, class Sched, bool ALIGN_EPI = false, bool SP2 = false, bool GATHER = false, bool FP8 = false>
; __device__ __forceinline__ void gemm_phase(PG8_LAS unsigned char* lds, const Gemm g, const Sched& S, const Epi& E, int tid_in  , const PG8_LAS unsigned* gofs = nullptr) {
;     ...
;             PG8_WAIT_V(8); PG8_WAIT_L(0); PG8_BAR; PG8_MMA(1, 0, At, B0); PG8_MMA(1, 1, At, B1); PG8_BAR; PG8_SCHED;
;             PG8_LDB(B0, 1, 0); PG8_LDB(B1, 1, 1); PG8_SCHED; PG8_LDA(At, 1, 0); PG8_STAGE_A(PG8_SA(0, 1), a2, 1, last);
;             PG8_WAIT_V(8); PG8_WAIT_L(0); PG8_BAR; PG8_MMA(0, 0, At, B0); PG8_MMA(0, 1, At, B1); PG8_BAR; PG8_SCHED;
	s_setprio 1
	s_waitcnt lgkmcnt(0)
	v_mfma_f32_16x16x32_bf16 v[64:67], v[142:145], v[178:181], v[64:67]
	v_mfma_f32_16x16x32_bf16 v[60:63], v[154:157], v[178:181], v[60:63]
	v_mfma_f32_16x16x32_bf16 v[56:59], v[142:145], v[186:189], v[56:59]
	v_mfma_f32_16x16x32_bf16 v[52:55], v[154:157], v[186:189], v[52:55]
	v_mfma_f32_16x16x32_bf16 v[44:47], v[142:145], v[194:197], v[44:47]
	v_mfma_f32_16x16x32_bf16 v[36:39], v[154:157], v[194:197], v[36:39]
	v_mfma_f32_16x16x32_bf16 v[28:31], v[142:145], v[202:205], v[28:31]
	v_mfma_f32_16x16x32_bf16 v[20:23], v[154:157], v[202:205], v[20:23]
	v_mfma_f32_16x16x32_bf16 v[64:67], v[146:149], v[182:185], v[64:67]
	v_mfma_f32_16x16x32_bf16 v[60:63], v[158:161], v[182:185], v[60:63]
	v_mfma_f32_16x16x32_bf16 v[56:59], v[146:149], v[190:193], v[56:59]
	v_mfma_f32_16x16x32_bf16 v[52:55], v[158:161], v[190:193], v[52:55]
	v_mfma_f32_16x16x32_bf16 v[44:47], v[146:149], v[198:201], v[44:47]
	v_mfma_f32_16x16x32_bf16 v[36:39], v[158:161], v[198:201], v[36:39]
	v_mfma_f32_16x16x32_bf16 v[28:31], v[146:149], v[218:221], v[28:31]
	v_mfma_f32_16x16x32_bf16 v[20:23], v[158:161], v[218:221], v[20:23]
	s_setprio 0
	s_setprio 1
	v_mfma_f32_16x16x32_bf16 v[48:51], v[162:165], v[178:181], v[48:51]
	v_mfma_f32_16x16x32_bf16 v[40:43], v[170:173], v[178:181], v[40:43]
	v_mfma_f32_16x16x32_bf16 v[32:35], v[162:165], v[186:189], v[32:35]
	v_mfma_f32_16x16x32_bf16 v[24:27], v[170:173], v[186:189], v[24:27]
	v_mfma_f32_16x16x32_bf16 v[16:19], v[162:165], v[194:197], v[16:19]
	v_mfma_f32_16x16x32_bf16 v[12:15], v[170:173], v[194:197], v[12:15]
	v_mfma_f32_16x16x32_bf16 v[8:11], v[162:165], v[202:205], v[8:11]
	v_mfma_f32_16x16x32_bf16 v[4:7], v[170:173], v[202:205], v[4:7]
	v_mfma_f32_16x16x32_bf16 v[48:51], v[166:169], v[182:185], v[48:51]
	v_mfma_f32_16x16x32_bf16 v[40:43], v[174:177], v[182:185], v[40:43]
	v_mfma_f32_16x16x32_bf16 v[32:35], v[166:169], v[190:193], v[32:35]
	v_mfma_f32_16x16x32_bf16 v[24:27], v[174:177], v[190:193], v[24:27]
	v_mfma_f32_16x16x32_bf16 v[16:19], v[166:169], v[198:201], v[16:19]
	v_mfma_f32_16x16x32_bf16 v[12:15], v[174:177], v[198:201], v[12:15]
	v_mfma_f32_16x16x32_bf16 v[8:11], v[166:169], v[218:221], v[8:11]
	v_mfma_f32_16x16x32_bf16 v[4:7], v[174:177], v[218:221], v[4:7]
	s_setprio 0
	s_barrier
	s_add_i32 s47, 0, 0x18000
	v_add_u32_e32 v153, s47, v150
	s_add_i32 s48, 0, 0x1c000
	ds_read_b128 v[142:145], v153
	ds_read_b128 v[146:149], v153 offset:1024
	ds_read_b128 v[154:157], v153 offset:2048
	ds_read_b128 v[158:161], v153 offset:3072
	v_add_u32_e32 v153, s48, v150
	ds_read_b128 v[162:165], v153
	ds_read_b128 v[166:169], v153 offset:1024
	ds_read_b128 v[170:173], v153 offset:2048
	ds_read_b128 v[174:177], v153 offset:3072
	s_add_u32 s20, s20, s0
	s_addc_u32 s21, s21, s1
	s_mov_b32 m0, s28
	v_lshl_add_u64 v[232:233], s[20:21], 0, v[136:137]
	ds_read_b128 v[178:181], v152 offset:32768
	ds_read_b128 v[182:185], v152 offset:33792
	ds_read_b128 v[186:189], v152 offset:34816
	ds_read_b128 v[190:193], v152 offset:35840
	ds_read_b128 v[194:197], v152 offset:36864
	ds_read_b128 v[198:201], v152 offset:37888
	ds_read_b128 v[202:205], v152 offset:38912
	ds_read_b128 v[218:221], v152 offset:39936
	global_load_lds_dwordx4 v[232:233], off
	v_lshl_add_u64 v[232:233], s[20:21], 0, v[132:133]
	s_mov_b32 m0, s29
	s_nop 0
	global_load_lds_dwordx4 v[232:233], off
	s_waitcnt vmcnt(8)
	s_waitcnt lgkmcnt(0)
	s_barrier
	s_setprio 1
	s_waitcnt lgkmcnt(0)
	v_mfma_f32_16x16x32_bf16 v[128:131], v[142:145], v[178:181], v[128:131]
	v_mfma_f32_16x16x32_bf16 v[124:127], v[154:157], v[178:181], v[124:127]
	v_mfma_f32_16x16x32_bf16 v[120:123], v[142:145], v[186:189], v[120:123]
	v_mfma_f32_16x16x32_bf16 v[116:119], v[154:157], v[186:189], v[116:119]
	v_mfma_f32_16x16x32_bf16 v[108:111], v[142:145], v[194:197], v[108:111]
	v_mfma_f32_16x16x32_bf16 v[100:103], v[154:157], v[194:197], v[100:103]
	v_mfma_f32_16x16x32_bf16 v[92:95], v[142:145], v[202:205], v[92:95]
	v_mfma_f32_16x16x32_bf16 v[84:87], v[154:157], v[202:205], v[84:87]
	v_mfma_f32_16x16x32_bf16 v[128:131], v[146:149], v[182:185], v[128:131]
	v_mfma_f32_16x16x32_bf16 v[124:127], v[158:161], v[182:185], v[124:127]
	v_mfma_f32_16x16x32_bf16 v[120:123], v[146:149], v[190:193], v[120:123]
	v_mfma_f32_16x16x32_bf16 v[116:119], v[158:161], v[190:193], v[116:119]
	v_mfma_f32_16x16x32_bf16 v[108:111], v[146:149], v[198:201], v[108:111]
	v_mfma_f32_16x16x32_bf16 v[100:103], v[158:161], v[198:201], v[100:103]
	v_mfma_f32_16x16x32_bf16 v[92:95], v[146:149], v[218:221], v[92:95]
	v_mfma_f32_16x16x32_bf16 v[84:87], v[158:161], v[218:221], v[84:87]
	s_setprio 0
	s_setprio 1
	v_mfma_f32_16x16x32_bf16 v[112:115], v[162:165], v[178:181], v[112:115]
	v_mfma_f32_16x16x32_bf16 v[104:107], v[170:173], v[178:181], v[104:107]
	v_mfma_f32_16x16x32_bf16 v[96:99], v[162:165], v[186:189], v[96:99]
	v_mfma_f32_16x16x32_bf16 v[88:91], v[170:173], v[186:189], v[88:91]
	v_mfma_f32_16x16x32_bf16 v[80:83], v[162:165], v[194:197], v[80:83]
	v_mfma_f32_16x16x32_bf16 v[76:79], v[170:173], v[194:197], v[76:79]
	v_mfma_f32_16x16x32_bf16 v[72:75], v[162:165], v[202:205], v[72:75]
	v_mfma_f32_16x16x32_bf16 v[68:71], v[170:173], v[202:205], v[68:71]
	v_mfma_f32_16x16x32_bf16 v[112:115], v[166:169], v[182:185], v[112:115]
	v_mfma_f32_16x16x32_bf16 v[104:107], v[174:177], v[182:185], v[104:107]
	v_mfma_f32_16x16x32_bf16 v[96:99], v[166:169], v[190:193], v[96:99]
	v_mfma_f32_16x16x32_bf16 v[88:91], v[174:177], v[190:193], v[88:91]
	v_mfma_f32_16x16x32_bf16 v[80:83], v[166:169], v[198:201], v[80:83]
	v_mfma_f32_16x16x32_bf16 v[76:79], v[174:177], v[198:201], v[76:79]
	v_mfma_f32_16x16x32_bf16 v[72:75], v[166:169], v[218:221], v[72:75]
	v_mfma_f32_16x16x32_bf16 v[68:71], v[174:177], v[218:221], v[68:71]
	s_setprio 0
	s_barrier
; #define PG8_STAGE(bufoff, gbase, voff) do { _Pragma("unroll") for (int _i = 0; _i < 2; ++_i) \
;         __builtin_amdgcn_global_load_lds((const unsigned*)((const char*)(gbase) + (voff)[_i]), (PG8_LAS unsigned*)(lds + (bufoff) + ldsw + _i * 8192), 16, 0, 0); } while (0)
; #define PG8_STAGE_A(bufoff, ptr, h, nx) do { if constexpr (GATHER) { const int ub_ = ((nx) ? gnext : ui) * 256 + (h) * 128; unsigned vv_[2]; _Pragma("unroll") for (int _j = 0; _j < 2; ++_j) vv_[_j] = gofs[ub_ + gL[_j]] + (unsigned)gC[_j]; PG8_STAGE(bufoff, ptr, vv_); } \
;         else { PG8_STAGE(bufoff, (ptr) + (size_t)(h) * hstep, voffA); } } while (0)
; #define PG8_LDA(dst, b, h) do { _Pragma("unroll") for (int m = 0; m < 4; ++m) _Pragma("unroll") for (int k = 0; k < 2; ++k) dst[m][k] = *(const PG8_LAS bf16x8*)(lds + PG8_SA(b, h) + aoff + m * 2048 + k * 1024); } while (0)
; #define PG8_WAIT_V(n) asm volatile("s_waitcnt vmcnt(" #n ")" ::: "memory")
; #define PG8_WAIT_L(n) asm volatile("s_waitcnt lgkmcnt(" #n ")" ::: "memory")
; #define PG8_BAR __builtin_amdgcn_s_barrier()
; #define PG8_SCHED __builtin_amdgcn_sched_barrier(0)
; template <class Epi, class Sched, bool ALIGN_EPI = false, bool SP2 = false, bool GATHER = false, bool FP8 = false>
; __device__ __forceinline__ void gemm_phase(PG8_LAS unsigned char* lds, const Gemm g, const Sched& S, const Epi& E, int tid_in  , const PG8_LAS unsigned* gofs = nullptr) {
;     ...
;         for (int t = 0; t < nt; t += 2) {
;             const bool last = (t == nt - 2);
;             const char* a1 = cA + (size_t)(t + 1) * kstep;
;             const char* a2 = last ? nA : cA + (size_t)(t + 2) * kstep; const char* b2 = last ? nB : cB + (size_t)(t + 2) * kstep;
;             const char* a3 = a2 + kstep; const char* b3 = b2 + kstep;
;     ...
;             PG8_LDA(At, 1, 1); PG8_STAGE(PG8_SB(1, 0), b3, voffB); PG8_STAGE(PG8_SB(1, 1), b3 + hstep, voffB); PG8_STAGE_A(PG8_SA(1, 0), a3, 0, last);
;             PG8_WAIT_V(8); PG8_WAIT_L(0); PG8_BAR; PG8_MMA(1, 0, At, B0); PG8_MMA(1, 1, At, B1); PG8_BAR; PG8_SCHED;
	s_add_i32 s20, s47, s24
	v_lshl_add_u64 v[208:209], v[208:209], 0, s[38:39]
	s_mov_b32 m0, s20
	ds_read_b128 v[178:181], v152 offset:49152
	ds_read_b128 v[182:185], v152 offset:50176
	ds_read_b128 v[186:189], v152 offset:51200
	ds_read_b128 v[190:193], v152 offset:52224
	ds_read_b128 v[194:197], v152 offset:53248
	ds_read_b128 v[198:201], v152 offset:54272
	ds_read_b128 v[202:205], v152 offset:55296
	ds_read_b128 v[218:221], v152 offset:56320
	global_load_lds_dwordx4 v[208:209], off
	v_lshl_add_u64 v[208:209], v[222:223], 0, s[38:39]
	s_add_i32 m0, s20, 0x2000
	s_add_i32 s20, s48, s24
	global_load_lds_dwordx4 v[208:209], off
	v_lshl_add_u64 v[208:209], v[224:225], 0, s[38:39]
	s_mov_b32 m0, s20
	s_nop 0
	global_load_lds_dwordx4 v[208:209], off
	v_lshl_add_u64 v[208:209], v[226:227], 0, s[38:39]
	s_add_i32 m0, s20, 0x2000
	s_nop 0
	global_load_lds_dwordx4 v[208:209], off
	v_lshl_add_u64 v[208:209], v[228:229], 0, s[38:39]
	s_mov_b32 m0, s36
	s_nop 0
	global_load_lds_dwordx4 v[208:209], off
	v_lshl_add_u64 v[208:209], v[230:231], 0, s[38:39]
	s_mov_b32 m0, s37
	s_nop 0
	global_load_lds_dwordx4 v[208:209], off
	s_waitcnt vmcnt(8)
	s_waitcnt lgkmcnt(0)
	s_barrier
	s_setprio 1
	s_waitcnt lgkmcnt(0)
	v_mfma_f32_16x16x32_bf16 v[64:67], v[142:145], v[178:181], v[64:67]
	s_add_u32 s18, s18, 0x100
	v_mfma_f32_16x16x32_bf16 v[60:63], v[154:157], v[178:181], v[60:63]
	s_addc_u32 s19, s19, 0
	v_mfma_f32_16x16x32_bf16 v[56:59], v[142:145], v[186:189], v[56:59]
	s_add_u32 s44, s44, 0x100
	v_mfma_f32_16x16x32_bf16 v[52:55], v[154:157], v[186:189], v[52:55]
	s_addc_u32 s45, s45, 0
	v_mfma_f32_16x16x32_bf16 v[44:47], v[142:145], v[194:197], v[44:47]
	s_cmp_ge_i32 s46, s34
	v_mfma_f32_16x16x32_bf16 v[36:39], v[154:157], v[194:197], v[36:39]
	s_cselect_b32 vcc_lo, 1, 0
	v_mfma_f32_16x16x32_bf16 v[28:31], v[142:145], v[202:205], v[28:31]
	s_mov_b32 s20, s46
	v_mfma_f32_16x16x32_bf16 v[20:23], v[154:157], v[202:205], v[20:23]
	s_add_i32 s46, s20, 2
	v_mfma_f32_16x16x32_bf16 v[64:67], v[146:149], v[182:185], v[64:67]
	s_add_u32 s47, s18, 0x80
	v_mfma_f32_16x16x32_bf16 v[60:63], v[158:161], v[182:185], v[60:63]
	s_addc_u32 s21, s19, 0
	v_mfma_f32_16x16x32_bf16 v[56:59], v[146:149], v[190:193], v[56:59]
	s_add_i32 s50, 0, 0x10000
	v_mfma_f32_16x16x32_bf16 v[52:55], v[158:161], v[190:193], v[52:55]
	s_cmp_eq_u32 s40, s20
	v_mfma_f32_16x16x32_bf16 v[44:47], v[146:149], v[198:201], v[44:47]
	s_cselect_b32 s21, s5, s21
	v_mfma_f32_16x16x32_bf16 v[36:39], v[158:161], v[198:201], v[36:39]
	s_cselect_b32 s20, s4, s47
	v_mfma_f32_16x16x32_bf16 v[28:31], v[146:149], v[218:221], v[28:31]
	s_cselect_b32 s49, s17, s45
	v_mfma_f32_16x16x32_bf16 v[20:23], v[158:161], v[218:221], v[20:23]
	s_cselect_b32 s48, s16, s44
	s_setprio 0
	s_setprio 1
	v_mfma_f32_16x16x32_bf16 v[48:51], v[162:165], v[178:181], v[48:51]
	s_add_i32 s47, 0, 0x14000
	v_mfma_f32_16x16x32_bf16 v[40:43], v[170:173], v[178:181], v[40:43]
	v_mfma_f32_16x16x32_bf16 v[32:35], v[162:165], v[186:189], v[32:35]
	v_mfma_f32_16x16x32_bf16 v[24:27], v[170:173], v[186:189], v[24:27]
	v_mfma_f32_16x16x32_bf16 v[16:19], v[162:165], v[194:197], v[16:19]
	v_mfma_f32_16x16x32_bf16 v[12:15], v[170:173], v[194:197], v[12:15]
	v_mfma_f32_16x16x32_bf16 v[8:11], v[162:165], v[202:205], v[8:11]
	v_mfma_f32_16x16x32_bf16 v[4:7], v[170:173], v[202:205], v[4:7]
	v_mfma_f32_16x16x32_bf16 v[48:51], v[166:169], v[182:185], v[48:51]
	v_mfma_f32_16x16x32_bf16 v[40:43], v[174:177], v[182:185], v[40:43]
	v_mfma_f32_16x16x32_bf16 v[32:35], v[166:169], v[190:193], v[32:35]
	v_mfma_f32_16x16x32_bf16 v[24:27], v[174:177], v[190:193], v[24:27]
	v_mfma_f32_16x16x32_bf16 v[16:19], v[166:169], v[198:201], v[16:19]
	v_mfma_f32_16x16x32_bf16 v[12:15], v[174:177], v[198:201], v[12:15]
	v_mfma_f32_16x16x32_bf16 v[8:11], v[166:169], v[218:221], v[8:11]
	v_mfma_f32_16x16x32_bf16 v[4:7], v[174:177], v[218:221], v[4:7]
	s_setprio 0
	s_barrier
;     __device__ __forceinline__ void operator()(const f32x4 (&acc)[2][2][4][2], const Unit& u, int wr, int wc, int fr, int fq) const {
;     ...
;             for (int n = 0; n < 2; ++n) bv[bj][n] = bias ? *(const f32x4*)(bias + bcol0 + bj * HALF + 4 * n) : (f32x4){0.f, 0.f, 0.f, 0.f};
; #pragma unroll
;         for (int ai = 0; ai < 2; ++ai)
; #pragma unroll
;             for (int m = 0; m < 4; ++m) { bf16_t* rowp = base + (size_t)(row0 + ai * HALF + m * 16) * ldc + col0;
; #pragma unroll
;                 for (int bj = 0; bj < 2; ++bj) { f32x4 v0 = acc[ai][bj][m][0] + bv[bj][0], v1 = acc[ai][bj][m][1] + bv[bj][1];
; template <class Epi, class Sched, bool ALIGN_EPI = false, bool SP2 = false, bool GATHER = false, bool FP8 = false>
; __device__ __forceinline__ void gemm_phase(PG8_LAS unsigned char* lds, const Gemm g, const Sched& S, const Epi& E, int tid_in  , const PG8_LAS unsigned* gofs = nullptr) {
;     ...
;         for (int t = 0; t < nt; t += 2) {
;             const bool last = (t == nt - 2);
;             const char* a1 = cA + (size_t)(t + 1) * kstep;
;             const char* a2 = last ? nA : cA + (size_t)(t + 2) * kstep; const char* b2 = last ? nB : cB + (size_t)(t + 2) * kstep;
;             const char* a3 = a2 + kstep; const char* b3 = b2 + kstep;
	s_cmp_eq_u32 vcc_lo, 0
	s_cbranch_scc1 .Lkrot2_body
	v_pk_add_f32 v[130:131], v[130:131], 0 op_sel_hi:[1,0]
	v_pk_add_f32 v[128:129], v[128:129], 0 op_sel_hi:[1,0]
	v_pk_add_f32 v[126:127], v[126:127], 0 op_sel_hi:[1,0]
	v_pk_add_f32 v[124:125], v[124:125], 0 op_sel_hi:[1,0]
	v_pk_add_f32 v[142:143], v[114:115], 0 op_sel_hi:[1,0]
	v_pk_add_f32 v[144:145], v[112:113], 0 op_sel_hi:[1,0]
	v_pk_add_f32 v[146:147], v[106:107], 0 op_sel_hi:[1,0]
	v_pk_add_f32 v[148:149], v[104:105], 0 op_sel_hi:[1,0]
	v_pk_add_f32 v[104:105], v[122:123], 0 op_sel_hi:[1,0]
	v_pk_add_f32 v[106:107], v[120:121], 0 op_sel_hi:[1,0]
	v_pk_add_f32 v[112:113], v[118:119], 0 op_sel_hi:[1,0]
	v_pk_add_f32 v[114:115], v[116:117], 0 op_sel_hi:[1,0]
	v_pk_add_f32 v[116:117], v[98:99], 0 op_sel_hi:[1,0]
	v_pk_add_f32 v[118:119], v[96:97], 0 op_sel_hi:[1,0]
	v_pk_add_f32 v[120:121], v[90:91], 0 op_sel_hi:[1,0]
	v_pk_add_f32 v[122:123], v[88:89], 0 op_sel_hi:[1,0]
	v_pk_add_f32 v[88:89], v[110:111], 0 op_sel_hi:[1,0]
	v_pk_add_f32 v[90:91], v[108:109], 0 op_sel_hi:[1,0]
	v_pk_add_f32 v[96:97], v[102:103], 0 op_sel_hi:[1,0]
	v_pk_add_f32 v[98:99], v[100:101], 0 op_sel_hi:[1,0]
	v_pk_add_f32 v[100:101], v[82:83], 0 op_sel_hi:[1,0]
	v_pk_add_f32 v[102:103], v[80:81], 0 op_sel_hi:[1,0]
	v_pk_add_f32 v[108:109], v[78:79], 0 op_sel_hi:[1,0]
	v_pk_add_f32 v[110:111], v[76:77], 0 op_sel_hi:[1,0]
	v_pk_add_f32 v[76:77], v[94:95], 0 op_sel_hi:[1,0]
	v_pk_add_f32 v[78:79], v[92:93], 0 op_sel_hi:[1,0]
	v_pk_add_f32 v[80:81], v[86:87], 0 op_sel_hi:[1,0]
	v_pk_add_f32 v[82:83], v[84:85], 0 op_sel_hi:[1,0]
	v_pk_add_f32 v[74:75], v[74:75], 0 op_sel_hi:[1,0]
	v_pk_add_f32 v[72:73], v[72:73], 0 op_sel_hi:[1,0]
	v_pk_add_f32 v[70:71], v[70:71], 0 op_sel_hi:[1,0]
	v_pk_add_f32 v[68:69], v[68:69], 0 op_sel_hi:[1,0]
	v_pk_add_f32 v[66:67], v[66:67], 0 op_sel_hi:[1,0]
	v_pk_add_f32 v[64:65], v[64:65], 0 op_sel_hi:[1,0]
	v_pk_add_f32 v[62:63], v[62:63], 0 op_sel_hi:[1,0]
	v_pk_add_f32 v[60:61], v[60:61], 0 op_sel_hi:[1,0]
	v_pk_add_f32 v[84:85], v[50:51], 0 op_sel_hi:[1,0]
	v_pk_add_f32 v[86:87], v[48:49], 0 op_sel_hi:[1,0]
	v_pk_add_f32 v[92:93], v[42:43], 0 op_sel_hi:[1,0]
	v_pk_add_f32 v[94:95], v[40:41], 0 op_sel_hi:[1,0]
	v_pk_add_f32 v[40:41], v[58:59], 0 op_sel_hi:[1,0]
	v_pk_add_f32 v[42:43], v[56:57], 0 op_sel_hi:[1,0]
	v_pk_add_f32 v[48:49], v[54:55], 0 op_sel_hi:[1,0]
	v_pk_add_f32 v[50:51], v[52:53], 0 op_sel_hi:[1,0]
	v_pk_add_f32 v[52:53], v[34:35], 0 op_sel_hi:[1,0]
	v_pk_add_f32 v[54:55], v[32:33], 0 op_sel_hi:[1,0]
	v_pk_add_f32 v[56:57], v[26:27], 0 op_sel_hi:[1,0]
	v_pk_add_f32 v[58:59], v[24:25], 0 op_sel_hi:[1,0]
	v_pk_add_f32 v[24:25], v[46:47], 0 op_sel_hi:[1,0]
	v_pk_add_f32 v[26:27], v[44:45], 0 op_sel_hi:[1,0]
	v_pk_add_f32 v[32:33], v[38:39], 0 op_sel_hi:[1,0]
	v_pk_add_f32 v[34:35], v[36:37], 0 op_sel_hi:[1,0]
	v_pk_add_f32 v[36:37], v[18:19], 0 op_sel_hi:[1,0]
	v_pk_add_f32 v[38:39], v[16:17], 0 op_sel_hi:[1,0]
	v_pk_add_f32 v[44:45], v[14:15], 0 op_sel_hi:[1,0]
	v_pk_add_f32 v[46:47], v[12:13], 0 op_sel_hi:[1,0]
	v_pk_add_f32 v[12:13], v[30:31], 0 op_sel_hi:[1,0]
	v_pk_add_f32 v[14:15], v[28:29], 0 op_sel_hi:[1,0]
	v_pk_add_f32 v[16:17], v[22:23], 0 op_sel_hi:[1,0]
	v_pk_add_f32 v[18:19], v[20:21], 0 op_sel_hi:[1,0]
	v_pk_add_f32 v[10:11], v[10:11], 0 op_sel_hi:[1,0]
	v_pk_add_f32 v[8:9], v[8:9], 0 op_sel_hi:[1,0]
	v_pk_add_f32 v[6:7], v[6:7], 0 op_sel_hi:[1,0]
	v_pk_add_f32 v[4:5], v[4:5], 0 op_sel_hi:[1,0]

; #define PG8_STAGE(bufoff, gbase, voff) do { _Pragma("unroll") for (int _i = 0; _i < 2; ++_i) \
;         __builtin_amdgcn_global_load_lds((const unsigned*)((const char*)(gbase) + (voff)[_i]), (PG8_LAS unsigned*)(lds + (bufoff) + ldsw + _i * 8192), 16, 0, 0); } while (0)
; #define PG8_STAGE_A(bufoff, ptr, h, nx) do { if constexpr (GATHER) { const int ub_ = ((nx) ? gnext : ui) * 256 + (h) * 128; unsigned vv_[2]; _Pragma("unroll") for (int _j = 0; _j < 2; ++_j) vv_[_j] = gofs[ub_ + gL[_j]] + (unsigned)gC[_j]; PG8_STAGE(bufoff, ptr, vv_); } \
;         else { PG8_STAGE(bufoff, (ptr) + (size_t)(h) * hstep, voffA); } } while (0)
; #define PG8_LDA(dst, b, h) do { _Pragma("unroll") for (int m = 0; m < 4; ++m) _Pragma("unroll") for (int k = 0; k < 2; ++k) dst[m][k] = *(const PG8_LAS bf16x8*)(lds + PG8_SA(b, h) + aoff + m * 2048 + k * 1024); } while (0)
; #define PG8_LDB(dst, b, h) do { _Pragma("unroll") for (int n = 0; n < 2; ++n) _Pragma("unroll") for (int k = 0; k < 2; ++k) dst[n][k] = *(const PG8_LAS bf16x8*)(lds + PG8_SB(b, h) + boff + n * 2048 + k * 1024); } while (0)
; #define PG8_WAIT_V(n) asm volatile("s_waitcnt vmcnt(" #n ")" ::: "memory")
; #define PG8_WAIT_L(n) asm volatile("s_waitcnt lgkmcnt(" #n ")" ::: "memory")
; #define PG8_BAR __builtin_amdgcn_s_barrier()
; #define PG8_SCHED __builtin_amdgcn_sched_barrier(0)
; template <class Epi, class Sched, bool ALIGN_EPI = false, bool SP2 = false, bool GATHER = false, bool FP8 = false>
; __device__ __forceinline__ void gemm_phase(PG8_LAS unsigned char* lds, const Gemm g, const Sched& S, const Epi& E, int tid_in  , const PG8_LAS unsigned* gofs = nullptr) {
;     ...
;             PG8_LDB(B0, 0, 0); PG8_LDB(B1, 0, 1); PG8_SCHED; PG8_LDA(At, 0, 0); PG8_STAGE_A(PG8_SA(1, 1), a1, 1, false);
;             PG8_WAIT_V(8); PG8_WAIT_L(0); PG8_BAR; PG8_MMA(0, 0, At, B0); PG8_MMA(0, 1, At, B1); PG8_BAR; PG8_SCHED;
;             PG8_LDA(At, 0, 1); PG8_STAGE(PG8_SB(0, 0), b2, voffB); PG8_STAGE(PG8_SB(0, 1), b2 + hstep, voffB); PG8_STAGE_A(PG8_SA(0, 0), a2, 0, last);
;             PG8_WAIT_V(8); PG8_WAIT_L(0); PG8_BAR; PG8_MMA(1, 0, At, B0); PG8_MMA(1, 1, At, B1); PG8_BAR; PG8_SCHED;
;             PG8_LDB(B0, 1, 0); PG8_LDB(B1, 1, 1); PG8_SCHED; PG8_LDA(At, 1, 0); PG8_STAGE_A(PG8_SA(0, 1), a2, 1, last);
;             PG8_WAIT_V(8); PG8_WAIT_L(0); PG8_BAR; PG8_MMA(0, 0, At, B0); PG8_MMA(0, 1, At, B1); PG8_BAR; PG8_SCHED;
.Lkrot3_body:
	v_add_u32_e32 v4, s75, v187
	v_add_u32_e32 v8, s76, v187
	ds_read_b128 v[28:31], v4
	ds_read_b128 v[32:35], v4 offset:1024
	ds_read_b128 v[20:23], v4 offset:2048
	ds_read_b128 v[24:27], v4 offset:3072
	ds_read_b128 v[12:15], v8
	ds_read_b128 v[16:19], v8 offset:1024
	ds_read_b128 v[4:7], v8 offset:2048
	ds_read_b128 v[8:11], v8 offset:3072
	v_lshl_add_u64 v[182:183], s[42:43], 0, v[170:171]
	s_add_i32 m0, s58, 0xc000
	ds_read_b128 v[174:177], v189
	ds_read_b128 v[178:181], v189 offset:1024
	ds_read_b128 v[190:193], v189 offset:2048
	ds_read_b128 v[194:197], v189 offset:3072
	ds_read_b128 v[218:221], v189 offset:4096
	ds_read_b128 v[222:225], v189 offset:5120
	ds_read_b128 v[226:229], v189 offset:6144
	ds_read_b128 v[230:233], v189 offset:7168
	global_load_lds_dwordx4 v[182:183], off
	v_lshl_add_u64 v[182:183], s[42:43], 0, v[172:173]
	s_add_i32 m0, s58, 0xe000
	s_nop 0
	global_load_lds_dwordx4 v[182:183], off
	s_waitcnt vmcnt(8)
	s_waitcnt lgkmcnt(0)
	s_barrier
	s_setprio 1
	s_waitcnt lgkmcnt(0)
	v_mfma_f32_16x16x128_f8f6f4 v[160:163], v[28:35], v[174:181], v[160:163]
	v_mfma_f32_16x16x128_f8f6f4 v[156:159], v[20:27], v[174:181], v[156:159]
	v_mfma_f32_16x16x128_f8f6f4 v[152:155], v[28:35], v[190:197], v[152:155]
	v_mfma_f32_16x16x128_f8f6f4 v[148:151], v[20:27], v[190:197], v[148:151]
	v_mfma_f32_16x16x128_f8f6f4 v[140:143], v[28:35], v[218:225], v[140:143]
	v_mfma_f32_16x16x128_f8f6f4 v[132:135], v[20:27], v[218:225], v[132:135]
	v_mfma_f32_16x16x128_f8f6f4 v[124:127], v[28:35], v[226:233], v[124:127]
	v_mfma_f32_16x16x128_f8f6f4 v[116:119], v[20:27], v[226:233], v[116:119]
	s_setprio 0
	s_setprio 1
	v_mfma_f32_16x16x128_f8f6f4 v[144:147], v[12:19], v[174:181], v[144:147]
	v_mfma_f32_16x16x128_f8f6f4 v[136:139], v[4:11], v[174:181], v[136:139]
	v_mfma_f32_16x16x128_f8f6f4 v[128:131], v[12:19], v[190:197], v[128:131]
	v_mfma_f32_16x16x128_f8f6f4 v[120:123], v[4:11], v[190:197], v[120:123]
	v_mfma_f32_16x16x128_f8f6f4 v[112:115], v[12:19], v[218:225], v[112:115]
	v_mfma_f32_16x16x128_f8f6f4 v[108:111], v[4:11], v[218:225], v[108:111]
	v_mfma_f32_16x16x128_f8f6f4 v[104:107], v[12:19], v[226:233], v[104:107]
	v_mfma_f32_16x16x128_f8f6f4 v[100:103], v[4:11], v[226:233], v[100:103]
	s_setprio 0
	s_barrier
	s_add_i32 s75, s75, s57
	v_lshl_add_u64 v[174:175], s[46:47], 0, v[164:165]
	s_mov_b32 m0, s75
	ds_read_b128 v[190:193], v189 offset:16384
	ds_read_b128 v[194:197], v189 offset:17408
	ds_read_b128 v[218:221], v189 offset:18432
	ds_read_b128 v[222:225], v189 offset:19456
	ds_read_b128 v[226:229], v189 offset:20480
	ds_read_b128 v[230:233], v189 offset:21504
	ds_read_b128 v[234:237], v189 offset:22528
	ds_read_b128 v[238:241], v189 offset:23552
	global_load_lds_dwordx4 v[174:175], off
	s_add_i32 m0, s75, 0x2000
	v_lshl_add_u64 v[176:177], s[46:47], 0, v[168:169]
	s_add_u32 s46, s46, s6
	s_addc_u32 s47, s47, s7
	s_add_i32 s75, s76, s57
	global_load_lds_dwordx4 v[176:177], off
	v_lshl_add_u64 v[178:179], s[46:47], 0, v[164:165]
	s_mov_b32 m0, s75
	v_lshl_add_u64 v[180:181], s[46:47], 0, v[168:169]
	global_load_lds_dwordx4 v[178:179], off
	s_add_i32 m0, s75, 0x2000
	v_lshl_add_u64 v[182:183], s[44:45], 0, v[0:1]
	global_load_lds_dwordx4 v[180:181], off
	s_mov_b32 m0, s58
	v_lshl_add_u64 v[184:185], s[44:45], 0, v[166:167]
	global_load_lds_dwordx4 v[182:183], off
	s_mov_b32 m0, s59
	s_nop 0
	global_load_lds_dwordx4 v[184:185], off
	s_waitcnt vmcnt(8)
	s_waitcnt lgkmcnt(0)
	s_barrier
	s_setprio 1
	s_waitcnt lgkmcnt(0)
	v_mfma_f32_16x16x128_f8f6f4 v[96:99], v[28:35], v[190:197], v[96:99]
	v_mfma_f32_16x16x128_f8f6f4 v[92:95], v[20:27], v[190:197], v[92:95]
	v_mfma_f32_16x16x128_f8f6f4 v[88:91], v[28:35], v[218:225], v[88:91]
	v_mfma_f32_16x16x128_f8f6f4 v[84:87], v[20:27], v[218:225], v[84:87]
	v_mfma_f32_16x16x128_f8f6f4 v[76:79], v[28:35], v[226:233], v[76:79]
	v_mfma_f32_16x16x128_f8f6f4 v[68:71], v[20:27], v[226:233], v[68:71]
	v_mfma_f32_16x16x128_f8f6f4 v[60:63], v[28:35], v[234:241], v[60:63]
	v_mfma_f32_16x16x128_f8f6f4 v[52:55], v[20:27], v[234:241], v[52:55]
	s_setprio 0
	s_setprio 1
	v_mfma_f32_16x16x128_f8f6f4 v[80:83], v[12:19], v[190:197], v[80:83]
	v_mfma_f32_16x16x128_f8f6f4 v[72:75], v[4:11], v[190:197], v[72:75]
	v_mfma_f32_16x16x128_f8f6f4 v[64:67], v[12:19], v[218:225], v[64:67]
	v_mfma_f32_16x16x128_f8f6f4 v[56:59], v[4:11], v[218:225], v[56:59]
	v_mfma_f32_16x16x128_f8f6f4 v[48:51], v[12:19], v[226:233], v[48:51]
	v_mfma_f32_16x16x128_f8f6f4 v[44:47], v[4:11], v[226:233], v[44:47]
	v_mfma_f32_16x16x128_f8f6f4 v[40:43], v[12:19], v[234:241], v[40:43]
	v_mfma_f32_16x16x128_f8f6f4 v[36:39], v[4:11], v[234:241], v[36:39]
	s_setprio 0
	s_barrier
	s_add_i32 s46, 0, 0x18000
	s_add_i32 s47, 0, 0x1c000
	v_add_u32_e32 v16, s46, v187
	v_add_u32_e32 v32, s47, v187
	ds_read_b128 v[4:7], v16
	ds_read_b128 v[8:11], v16 offset:1024
	ds_read_b128 v[12:15], v16 offset:2048
	ds_read_b128 v[16:19], v16 offset:3072
	ds_read_b128 v[20:23], v32
	ds_read_b128 v[24:27], v32 offset:1024
	ds_read_b128 v[28:31], v32 offset:2048
	ds_read_b128 v[32:35], v32 offset:3072
	s_add_u32 s44, s44, s6
	s_addc_u32 s45, s45, s7
	s_mov_b32 m0, s60
	v_lshl_add_u64 v[198:199], s[44:45], 0, v[0:1]
	ds_read_b128 v[190:193], v189 offset:32768
	ds_read_b128 v[194:197], v189 offset:33792
	ds_read_b128 v[218:221], v189 offset:34816
	ds_read_b128 v[222:225], v189 offset:35840
	ds_read_b128 v[226:229], v189 offset:36864
	ds_read_b128 v[230:233], v189 offset:37888
	ds_read_b128 v[234:237], v189 offset:38912
	ds_read_b128 v[238:241], v189 offset:39936
	global_load_lds_dwordx4 v[198:199], off
	v_lshl_add_u64 v[198:199], s[44:45], 0, v[166:167]
	s_mov_b32 m0, s61
	s_nop 0
	global_load_lds_dwordx4 v[198:199], off
	s_waitcnt vmcnt(8)
	s_waitcnt lgkmcnt(0)
	s_barrier
; #define PG8_STAGE(bufoff, gbase, voff) do { _Pragma("unroll") for (int _i = 0; _i < 2; ++_i) \
;         __builtin_amdgcn_global_load_lds((const unsigned*)((const char*)(gbase) + (voff)[_i]), (PG8_LAS unsigned*)(lds + (bufoff) + ldsw + _i * 8192), 16, 0, 0); } while (0)
; #define PG8_STAGE_A(bufoff, ptr, h, nx) do { if constexpr (GATHER) { const int ub_ = ((nx) ? gnext : ui) * 256 + (h) * 128; unsigned vv_[2]; _Pragma("unroll") for (int _j = 0; _j < 2; ++_j) vv_[_j] = gofs[ub_ + gL[_j]] + (unsigned)gC[_j]; PG8_STAGE(bufoff, ptr, vv_); } \
;         else { PG8_STAGE(bufoff, (ptr) + (size_t)(h) * hstep, voffA); } } while (0)
; #define PG8_LDA(dst, b, h) do { _Pragma("unroll") for (int m = 0; m < 4; ++m) _Pragma("unroll") for (int k = 0; k < 2; ++k) dst[m][k] = *(const PG8_LAS bf16x8*)(lds + PG8_SA(b, h) + aoff + m * 2048 + k * 1024); } while (0)
; #define PG8_WAIT_V(n) asm volatile("s_waitcnt vmcnt(" #n ")" ::: "memory")
; #define PG8_WAIT_L(n) asm volatile("s_waitcnt lgkmcnt(" #n ")" ::: "memory")
; #define PG8_BAR __builtin_amdgcn_s_barrier()
; #define PG8_SCHED __builtin_amdgcn_sched_barrier(0)
; template <class Epi, class Sched, bool ALIGN_EPI = false, bool SP2 = false, bool GATHER = false, bool FP8 = false>
; __device__ __forceinline__ void gemm_phase(PG8_LAS unsigned char* lds, const Gemm g, const Sched& S, const Epi& E, int tid_in  , const PG8_LAS unsigned* gofs = nullptr) {
;     ...
;         for (int t = 0; t < nt; t += 2) {
;             const bool last = (t == nt - 2);
;             const char* a1 = cA + (size_t)(t + 1) * kstep;
;             const char* a2 = last ? nA : cA + (size_t)(t + 2) * kstep; const char* b2 = last ? nB : cB + (size_t)(t + 2) * kstep;
;             const char* a3 = a2 + kstep; const char* b3 = b2 + kstep;
;     ...
;             PG8_WAIT_V(8); PG8_WAIT_L(0); PG8_BAR; PG8_MMA(0, 0, At, B0); PG8_MMA(0, 1, At, B1); PG8_BAR; PG8_SCHED;
;             PG8_LDA(At, 1, 1); PG8_STAGE(PG8_SB(1, 0), b3, voffB); PG8_STAGE(PG8_SB(1, 1), b3 + hstep, voffB); PG8_STAGE_A(PG8_SA(1, 0), a3, 0, last);
;             PG8_WAIT_V(8); PG8_WAIT_L(0); PG8_BAR; PG8_MMA(1, 0, At, B0); PG8_MMA(1, 1, At, B1); PG8_BAR; PG8_SCHED;
	s_setprio 1
	s_waitcnt lgkmcnt(0)
	v_mfma_f32_16x16x128_f8f6f4 v[160:163], v[4:11], v[190:197], v[160:163]
	v_mfma_f32_16x16x128_f8f6f4 v[156:159], v[12:19], v[190:197], v[156:159]
	v_mfma_f32_16x16x128_f8f6f4 v[152:155], v[4:11], v[218:225], v[152:155]
	v_mfma_f32_16x16x128_f8f6f4 v[148:151], v[12:19], v[218:225], v[148:151]
	v_mfma_f32_16x16x128_f8f6f4 v[140:143], v[4:11], v[226:233], v[140:143]
	v_mfma_f32_16x16x128_f8f6f4 v[132:135], v[12:19], v[226:233], v[132:135]
	v_mfma_f32_16x16x128_f8f6f4 v[124:127], v[4:11], v[234:241], v[124:127]
	v_mfma_f32_16x16x128_f8f6f4 v[116:119], v[12:19], v[234:241], v[116:119]
	s_setprio 0
	s_setprio 1
	v_mfma_f32_16x16x128_f8f6f4 v[144:147], v[20:27], v[190:197], v[144:147]
	v_mfma_f32_16x16x128_f8f6f4 v[136:139], v[28:35], v[190:197], v[136:139]
	v_mfma_f32_16x16x128_f8f6f4 v[128:131], v[20:27], v[218:225], v[128:131]
	v_mfma_f32_16x16x128_f8f6f4 v[120:123], v[28:35], v[218:225], v[120:123]
	v_mfma_f32_16x16x128_f8f6f4 v[112:115], v[20:27], v[226:233], v[112:115]
	v_mfma_f32_16x16x128_f8f6f4 v[108:111], v[28:35], v[226:233], v[108:111]
	v_mfma_f32_16x16x128_f8f6f4 v[104:107], v[20:27], v[234:241], v[104:107]
	v_mfma_f32_16x16x128_f8f6f4 v[100:103], v[28:35], v[234:241], v[100:103]
	s_setprio 0
	s_barrier
	s_add_i32 s44, s46, s57
	v_lshl_add_u64 v[174:175], v[174:175], 0, s[38:39]
	s_mov_b32 m0, s44
	ds_read_b128 v[190:193], v189 offset:49152
	ds_read_b128 v[194:197], v189 offset:50176
	ds_read_b128 v[218:221], v189 offset:51200
	ds_read_b128 v[222:225], v189 offset:52224
	ds_read_b128 v[226:229], v189 offset:53248
	ds_read_b128 v[230:233], v189 offset:54272
	ds_read_b128 v[234:237], v189 offset:55296
	ds_read_b128 v[238:241], v189 offset:56320
	global_load_lds_dwordx4 v[174:175], off
	v_lshl_add_u64 v[174:175], v[176:177], 0, s[38:39]
	s_add_i32 m0, s44, 0x2000
	s_add_i32 s44, s47, s57
	global_load_lds_dwordx4 v[174:175], off
	v_lshl_add_u64 v[174:175], v[178:179], 0, s[38:39]
	s_mov_b32 m0, s44
	s_nop 0
	global_load_lds_dwordx4 v[174:175], off
	v_lshl_add_u64 v[174:175], v[180:181], 0, s[38:39]
	s_add_i32 m0, s44, 0x2000
	s_nop 0
	global_load_lds_dwordx4 v[174:175], off
	v_lshl_add_u64 v[174:175], v[182:183], 0, s[38:39]
	s_mov_b32 m0, s64
	s_nop 0
	global_load_lds_dwordx4 v[174:175], off
	v_lshl_add_u64 v[174:175], v[184:185], 0, s[38:39]
	s_mov_b32 m0, s65
	s_nop 0
	global_load_lds_dwordx4 v[174:175], off
	s_waitcnt vmcnt(8)
	s_waitcnt lgkmcnt(0)
	s_barrier
	s_setprio 1
	s_waitcnt lgkmcnt(0)
	v_mfma_f32_16x16x128_f8f6f4 v[96:99], v[4:11], v[190:197], v[96:99]
	s_add_u32 s42, s42, 0x100
	s_addc_u32 s43, s43, 0
	v_mfma_f32_16x16x128_f8f6f4 v[92:95], v[12:19], v[190:197], v[92:95]
	s_add_u32 s72, s72, 0x100
	s_addc_u32 s73, s73, 0
	v_mfma_f32_16x16x128_f8f6f4 v[88:91], v[4:11], v[218:225], v[88:91]
	s_cmp_ge_i32 s74, s63
	s_cselect_b32 vcc_lo, 1, 0
	v_mfma_f32_16x16x128_f8f6f4 v[84:87], v[12:19], v[218:225], v[84:87]
	s_mov_b32 s44, s74
	s_add_i32 s74, s44, 2
	v_mfma_f32_16x16x128_f8f6f4 v[76:79], v[4:11], v[226:233], v[76:79]
	s_add_u32 s46, s42, 0x80
	s_addc_u32 s45, s43, 0
	v_mfma_f32_16x16x128_f8f6f4 v[68:71], v[12:19], v[226:233], v[68:71]
	s_add_i32 s75, 0, 0x10000
	s_cmp_eq_u32 s66, s44
	v_mfma_f32_16x16x128_f8f6f4 v[60:63], v[4:11], v[234:241], v[60:63]
	s_cselect_b32 s45, s5, s45
	s_cselect_b32 s44, s4, s46
	v_mfma_f32_16x16x128_f8f6f4 v[52:55], v[12:19], v[234:241], v[52:55]
	s_cselect_b32 s47, s41, s73
	s_cselect_b32 s46, s40, s72
	s_setprio 0
	s_setprio 1
	v_mfma_f32_16x16x128_f8f6f4 v[80:83], v[20:27], v[190:197], v[80:83]
	s_add_i32 s76, 0, 0x14000
	v_mfma_f32_16x16x128_f8f6f4 v[72:75], v[28:35], v[190:197], v[72:75]
	v_mfma_f32_16x16x128_f8f6f4 v[64:67], v[20:27], v[218:225], v[64:67]
	v_mfma_f32_16x16x128_f8f6f4 v[56:59], v[28:35], v[218:225], v[56:59]
	v_mfma_f32_16x16x128_f8f6f4 v[48:51], v[20:27], v[226:233], v[48:51]
	v_mfma_f32_16x16x128_f8f6f4 v[44:47], v[28:35], v[226:233], v[44:47]
	v_mfma_f32_16x16x128_f8f6f4 v[40:43], v[20:27], v[234:241], v[40:43]
	v_mfma_f32_16x16x128_f8f6f4 v[36:39], v[28:35], v[234:241], v[36:39]
	s_setprio 0
	s_barrier
;     __device__ __forceinline__ void operator()(const f32x4 (&acc)[2][2][4][2], const Unit& u, int wr, int wc, int fr, int fq) const {
;     ...
;             for (int m = 0; m < 4; ++m) { const size_t off = (size_t)(row0 + ai * HALF + m * 16) * ldc + col0; float ssq = 0.f;
; #pragma unroll
;                 for (int bj = 0; bj < 2; ++bj) {
;                     const f32x4 o0 = b0[m][bj] + acc[ai][bj][m][0] * sc, o1 = b1[m][bj] + acc[ai][bj][m][1] * sc;
; template <class Epi, class Sched, bool ALIGN_EPI = false, bool SP2 = false, bool GATHER = false, bool FP8 = false>
; __device__ __forceinline__ void gemm_phase(PG8_LAS unsigned char* lds, const Gemm g, const Sched& S, const Epi& E, int tid_in  , const PG8_LAS unsigned* gofs = nullptr) {
;     ...
;         for (int t = 0; t < nt; t += 2) {
;             const bool last = (t == nt - 2);
;             const char* a1 = cA + (size_t)(t + 1) * kstep;
;             const char* a2 = last ? nA : cA + (size_t)(t + 2) * kstep; const char* b2 = last ? nB : cB + (size_t)(t + 2) * kstep;
;             const char* a3 = a2 + kstep; const char* b3 = b2 + kstep;
	s_cmp_eq_u32 vcc_lo, 0
	s_cbranch_scc1 .Lkrot3_body
	s_mov_b32 s42, 0x38800000
	v_pk_mul_f32 v[162:163], v[162:163], s[42:43] op_sel_hi:[1,0]
	v_pk_mul_f32 v[160:161], v[160:161], s[42:43] op_sel_hi:[1,0]
	v_pk_mul_f32 v[174:175], v[158:159], s[42:43] op_sel_hi:[1,0]
	v_pk_mul_f32 v[176:177], v[156:157], s[42:43] op_sel_hi:[1,0]
	v_pk_mul_f32 v[178:179], v[146:147], s[42:43] op_sel_hi:[1,0]
	v_pk_mul_f32 v[180:181], v[144:145], s[42:43] op_sel_hi:[1,0]
	v_pk_mul_f32 v[182:183], v[138:139], s[42:43] op_sel_hi:[1,0]
	v_pk_mul_f32 v[184:185], v[136:137], s[42:43] op_sel_hi:[1,0]
	v_pk_mul_f32 v[158:159], v[154:155], s[42:43] op_sel_hi:[1,0]
	v_pk_mul_f32 v[156:157], v[152:153], s[42:43] op_sel_hi:[1,0]
	v_pk_mul_f32 v[154:155], v[150:151], s[42:43] op_sel_hi:[1,0]
	v_pk_mul_f32 v[152:153], v[148:149], s[42:43] op_sel_hi:[1,0]
	v_pk_mul_f32 v[150:151], v[130:131], s[42:43] op_sel_hi:[1,0]
	v_pk_mul_f32 v[148:149], v[128:129], s[42:43] op_sel_hi:[1,0]
	v_pk_mul_f32 v[146:147], v[122:123], s[42:43] op_sel_hi:[1,0]
	v_pk_mul_f32 v[144:145], v[120:121], s[42:43] op_sel_hi:[1,0]
	v_pk_mul_f32 v[142:143], v[142:143], s[42:43] op_sel_hi:[1,0]
	v_pk_mul_f32 v[140:141], v[140:141], s[42:43] op_sel_hi:[1,0]
	v_pk_mul_f32 v[138:139], v[134:135], s[42:43] op_sel_hi:[1,0]
	v_pk_mul_f32 v[136:137], v[132:133], s[42:43] op_sel_hi:[1,0]
	v_pk_mul_f32 v[134:135], v[114:115], s[42:43] op_sel_hi:[1,0]
	v_pk_mul_f32 v[132:133], v[112:113], s[42:43] op_sel_hi:[1,0]
	v_pk_mul_f32 v[130:131], v[110:111], s[42:43] op_sel_hi:[1,0]
	v_pk_mul_f32 v[128:129], v[108:109], s[42:43] op_sel_hi:[1,0]
	v_pk_mul_f32 v[126:127], v[126:127], s[42:43] op_sel_hi:[1,0]
	v_pk_mul_f32 v[124:125], v[124:125], s[42:43] op_sel_hi:[1,0]
	v_pk_mul_f32 v[122:123], v[118:119], s[42:43] op_sel_hi:[1,0]
	v_pk_mul_f32 v[120:121], v[116:117], s[42:43] op_sel_hi:[1,0]
	v_pk_mul_f32 v[118:119], v[106:107], s[42:43] op_sel_hi:[1,0]
	v_pk_mul_f32 v[116:117], v[104:105], s[42:43] op_sel_hi:[1,0]
	v_pk_mul_f32 v[114:115], v[102:103], s[42:43] op_sel_hi:[1,0]
	v_pk_mul_f32 v[112:113], v[100:101], s[42:43] op_sel_hi:[1,0]
	v_pk_mul_f32 v[110:111], v[98:99], s[42:43] op_sel_hi:[1,0]
	v_pk_mul_f32 v[108:109], v[96:97], s[42:43] op_sel_hi:[1,0]
	v_pk_mul_f32 v[106:107], v[94:95], s[42:43] op_sel_hi:[1,0]
	v_pk_mul_f32 v[104:105], v[92:93], s[42:43] op_sel_hi:[1,0]
	v_pk_mul_f32 v[102:103], v[82:83], s[42:43] op_sel_hi:[1,0]
	v_pk_mul_f32 v[100:101], v[80:81], s[42:43] op_sel_hi:[1,0]
	v_pk_mul_f32 v[98:99], v[74:75], s[42:43] op_sel_hi:[1,0]
	v_pk_mul_f32 v[96:97], v[72:73], s[42:43] op_sel_hi:[1,0]
	v_pk_mul_f32 v[94:95], v[90:91], s[42:43] op_sel_hi:[1,0]
	v_pk_mul_f32 v[92:93], v[88:89], s[42:43] op_sel_hi:[1,0]
	v_pk_mul_f32 v[90:91], v[86:87], s[42:43] op_sel_hi:[1,0]
	v_pk_mul_f32 v[88:89], v[84:85], s[42:43] op_sel_hi:[1,0]
	v_pk_mul_f32 v[86:87], v[66:67], s[42:43] op_sel_hi:[1,0]
	v_pk_mul_f32 v[84:85], v[64:65], s[42:43] op_sel_hi:[1,0]
	v_pk_mul_f32 v[82:83], v[58:59], s[42:43] op_sel_hi:[1,0]
	v_pk_mul_f32 v[80:81], v[56:57], s[42:43] op_sel_hi:[1,0]
	v_pk_mul_f32 v[74:75], v[78:79], s[42:43] op_sel_hi:[1,0]
	v_pk_mul_f32 v[72:73], v[76:77], s[42:43] op_sel_hi:[1,0]
	v_pk_mul_f32 v[70:71], v[70:71], s[42:43] op_sel_hi:[1,0]
	v_pk_mul_f32 v[68:69], v[68:69], s[42:43] op_sel_hi:[1,0]
	v_pk_mul_f32 v[66:67], v[50:51], s[42:43] op_sel_hi:[1,0]
	v_pk_mul_f32 v[64:65], v[48:49], s[42:43] op_sel_hi:[1,0]
	v_pk_mul_f32 v[58:59], v[46:47], s[42:43] op_sel_hi:[1,0]
	v_pk_mul_f32 v[56:57], v[44:45], s[42:43] op_sel_hi:[1,0]
	v_pk_mul_f32 v[50:51], v[62:63], s[42:43] op_sel_hi:[1,0]
	v_pk_mul_f32 v[48:49], v[60:61], s[42:43] op_sel_hi:[1,0]
	v_pk_mul_f32 v[46:47], v[54:55], s[42:43] op_sel_hi:[1,0]
	v_pk_mul_f32 v[44:45], v[52:53], s[42:43] op_sel_hi:[1,0]
	v_pk_mul_f32 v[34:35], v[42:43], s[42:43] op_sel_hi:[1,0]
	v_pk_mul_f32 v[32:33], v[40:41], s[42:43] op_sel_hi:[1,0]
	v_pk_mul_f32 v[30:31], v[38:39], s[42:43] op_sel_hi:[1,0]
	v_pk_mul_f32 v[28:29], v[36:37], s[42:43] op_sel_hi:[1,0]

; #define PG8_STAGE(bufoff, gbase, voff) do { _Pragma("unroll") for (int _i = 0; _i < 2; ++_i) \
;         __builtin_amdgcn_global_load_lds((const unsigned*)((const char*)(gbase) + (voff)[_i]), (PG8_LAS unsigned*)(lds + (bufoff) + ldsw + _i * 8192), 16, 0, 0); } while (0)
; #define PG8_STAGE_A(bufoff, ptr, h, nx) do { if constexpr (GATHER) { const int ub_ = ((nx) ? gnext : ui) * 256 + (h) * 128; unsigned vv_[2]; _Pragma("unroll") for (int _j = 0; _j < 2; ++_j) vv_[_j] = gofs[ub_ + gL[_j]] + (unsigned)gC[_j]; PG8_STAGE(bufoff, ptr, vv_); } \
;         else { PG8_STAGE(bufoff, (ptr) + (size_t)(h) * hstep, voffA); } } while (0)
; #define PG8_LDA(dst, b, h) do { _Pragma("unroll") for (int m = 0; m < 4; ++m) _Pragma("unroll") for (int k = 0; k < 2; ++k) dst[m][k] = *(const PG8_LAS bf16x8*)(lds + PG8_SA(b, h) + aoff + m * 2048 + k * 1024); } while (0)
; #define PG8_LDB(dst, b, h) do { _Pragma("unroll") for (int n = 0; n < 2; ++n) _Pragma("unroll") for (int k = 0; k < 2; ++k) dst[n][k] = *(const PG8_LAS bf16x8*)(lds + PG8_SB(b, h) + boff + n * 2048 + k * 1024); } while (0)
; #define PG8_WAIT_V(n) asm volatile("s_waitcnt vmcnt(" #n ")" ::: "memory")
; #define PG8_WAIT_L(n) asm volatile("s_waitcnt lgkmcnt(" #n ")" ::: "memory")
; #define PG8_BAR __builtin_amdgcn_s_barrier()
; #define PG8_SCHED __builtin_amdgcn_sched_barrier(0)
; template <class Epi, class Sched, bool ALIGN_EPI = false, bool SP2 = false, bool GATHER = false, bool FP8 = false>
; __device__ __forceinline__ void gemm_phase(PG8_LAS unsigned char* lds, const Gemm g, const Sched& S, const Epi& E, int tid_in  , const PG8_LAS unsigned* gofs = nullptr) {
;     ...
;             PG8_LDB(B0, 0, 0); PG8_LDB(B1, 0, 1); PG8_SCHED; PG8_LDA(At, 0, 0); PG8_STAGE_A(PG8_SA(1, 1), a1, 1, false);
;             PG8_WAIT_V(8); PG8_WAIT_L(0); PG8_BAR; PG8_MMA(0, 0, At, B0); PG8_MMA(0, 1, At, B1); PG8_BAR; PG8_SCHED;
;             PG8_LDA(At, 0, 1); PG8_STAGE(PG8_SB(0, 0), b2, voffB); PG8_STAGE(PG8_SB(0, 1), b2 + hstep, voffB); PG8_STAGE_A(PG8_SA(0, 0), a2, 0, last);
;             PG8_WAIT_V(8); PG8_WAIT_L(0); PG8_BAR; PG8_MMA(1, 0, At, B0); PG8_MMA(1, 1, At, B1); PG8_BAR; PG8_SCHED;
.Lkrot4_body:
	v_add_u32_e32 v144, s76, v209
	v_add_u32_e32 v160, s73, v209
	ds_read_b128 v[132:135], v144
	ds_read_b128 v[136:139], v144 offset:1024
	ds_read_b128 v[140:143], v144 offset:2048
	ds_read_b128 v[144:147], v144 offset:3072
	ds_read_b128 v[148:151], v160
	ds_read_b128 v[152:155], v160 offset:1024
	ds_read_b128 v[156:159], v160 offset:2048
	ds_read_b128 v[160:163], v160 offset:3072
	v_lshl_add_u64 v[220:221], s[42:43], 0, v[186:187]
	s_add_i32 m0, s47, 0xc000
	ds_read_b128 v[164:167], v219
	ds_read_b128 v[168:171], v219 offset:1024
	ds_read_b128 v[172:175], v219 offset:2048
	ds_read_b128 v[176:179], v219 offset:3072
	ds_read_b128 v[190:193], v219 offset:4096
	ds_read_b128 v[194:197], v219 offset:5120
	ds_read_b128 v[198:201], v219 offset:6144
	ds_read_b128 v[202:205], v219 offset:7168
	global_load_lds_dwordx4 v[220:221], off
	v_lshl_add_u64 v[220:221], s[42:43], 0, v[188:189]
	s_add_i32 m0, s47, 0xe000
	s_nop 0
	global_load_lds_dwordx4 v[220:221], off
	s_waitcnt vmcnt(8)
	s_waitcnt lgkmcnt(0)
	s_barrier
	s_setprio 1
	s_waitcnt lgkmcnt(0)
	v_mfma_f32_16x16x32_bf16 v[124:127], v[132:135], v[164:167], v[124:127]
	v_mfma_f32_16x16x32_bf16 v[128:131], v[140:143], v[164:167], v[128:131]
	v_mfma_f32_16x16x32_bf16 v[112:115], v[132:135], v[172:175], v[112:115]
	v_mfma_f32_16x16x32_bf16 v[108:111], v[140:143], v[172:175], v[108:111]
	v_mfma_f32_16x16x32_bf16 v[96:99], v[132:135], v[190:193], v[96:99]
	v_mfma_f32_16x16x32_bf16 v[92:95], v[140:143], v[190:193], v[92:95]
	v_mfma_f32_16x16x32_bf16 v[80:83], v[132:135], v[198:201], v[80:83]
	v_mfma_f32_16x16x32_bf16 v[76:79], v[140:143], v[198:201], v[76:79]
	v_mfma_f32_16x16x32_bf16 v[124:127], v[136:139], v[168:171], v[124:127]
	v_mfma_f32_16x16x32_bf16 v[128:131], v[144:147], v[168:171], v[128:131]
	v_mfma_f32_16x16x32_bf16 v[112:115], v[136:139], v[176:179], v[112:115]
	v_mfma_f32_16x16x32_bf16 v[108:111], v[144:147], v[176:179], v[108:111]
	v_mfma_f32_16x16x32_bf16 v[96:99], v[136:139], v[194:197], v[96:99]
	v_mfma_f32_16x16x32_bf16 v[92:95], v[144:147], v[194:197], v[92:95]
	v_mfma_f32_16x16x32_bf16 v[80:83], v[136:139], v[202:205], v[80:83]
	v_mfma_f32_16x16x32_bf16 v[76:79], v[144:147], v[202:205], v[76:79]
	s_setprio 0
	s_setprio 1
	v_mfma_f32_16x16x32_bf16 v[120:123], v[148:151], v[164:167], v[120:123]
	v_mfma_f32_16x16x32_bf16 v[116:119], v[156:159], v[164:167], v[116:119]
	v_mfma_f32_16x16x32_bf16 v[104:107], v[148:151], v[172:175], v[104:107]
	v_mfma_f32_16x16x32_bf16 v[100:103], v[156:159], v[172:175], v[100:103]
	v_mfma_f32_16x16x32_bf16 v[88:91], v[148:151], v[190:193], v[88:91]
	v_mfma_f32_16x16x32_bf16 v[84:87], v[156:159], v[190:193], v[84:87]
	v_mfma_f32_16x16x32_bf16 v[72:75], v[148:151], v[198:201], v[72:75]
	v_mfma_f32_16x16x32_bf16 v[68:71], v[156:159], v[198:201], v[68:71]
	v_mfma_f32_16x16x32_bf16 v[120:123], v[152:155], v[168:171], v[120:123]
	v_mfma_f32_16x16x32_bf16 v[116:119], v[160:163], v[168:171], v[116:119]
	v_mfma_f32_16x16x32_bf16 v[104:107], v[152:155], v[176:179], v[104:107]
	v_mfma_f32_16x16x32_bf16 v[100:103], v[160:163], v[176:179], v[100:103]
	v_mfma_f32_16x16x32_bf16 v[88:91], v[152:155], v[194:197], v[88:91]
	v_mfma_f32_16x16x32_bf16 v[84:87], v[160:163], v[194:197], v[84:87]
	v_mfma_f32_16x16x32_bf16 v[72:75], v[152:155], v[202:205], v[72:75]
	v_mfma_f32_16x16x32_bf16 v[68:71], v[160:163], v[202:205], v[68:71]
	s_setprio 0
	s_barrier
	s_add_i32 s76, s76, s46
	v_lshl_add_u64 v[220:221], s[74:75], 0, v[180:181]
	s_mov_b32 m0, s76
	ds_read_b128 v[164:167], v219 offset:16384
	ds_read_b128 v[168:171], v219 offset:17408
	ds_read_b128 v[172:175], v219 offset:18432
	ds_read_b128 v[176:179], v219 offset:19456
	ds_read_b128 v[190:193], v219 offset:20480
	ds_read_b128 v[194:197], v219 offset:21504
	ds_read_b128 v[198:201], v219 offset:22528
	ds_read_b128 v[202:205], v219 offset:23552
	global_load_lds_dwordx4 v[220:221], off
	s_add_i32 m0, s76, 0x2000
	v_lshl_add_u64 v[222:223], s[74:75], 0, v[184:185]
	s_add_u32 s74, s74, s24
	s_addc_u32 s75, s75, s25
	s_add_i32 s73, s73, s46
	global_load_lds_dwordx4 v[222:223], off
	v_lshl_add_u64 v[224:225], s[74:75], 0, v[180:181]
	s_mov_b32 m0, s73
	v_lshl_add_u64 v[226:227], s[74:75], 0, v[184:185]
	global_load_lds_dwordx4 v[224:225], off
	s_add_i32 m0, s73, 0x2000
	v_lshl_add_u64 v[228:229], s[44:45], 0, v[0:1]
	global_load_lds_dwordx4 v[226:227], off
	s_mov_b32 m0, s47
	v_lshl_add_u64 v[230:231], s[44:45], 0, v[182:183]
	global_load_lds_dwordx4 v[228:229], off
	s_mov_b32 m0, s57
	s_nop 0
	global_load_lds_dwordx4 v[230:231], off
	s_waitcnt vmcnt(8)
	s_waitcnt lgkmcnt(0)
	s_barrier
; #define PG8_STAGE_A(bufoff, ptr, h, nx) do { if constexpr (GATHER) { const int ub_ = ((nx) ? gnext : ui) * 256 + (h) * 128; unsigned vv_[2]; _Pragma("unroll") for (int _j = 0; _j < 2; ++_j) vv_[_j] = gofs[ub_ + gL[_j]] + (unsigned)gC[_j]; PG8_STAGE(bufoff, ptr, vv_); } \
;         else { PG8_STAGE(bufoff, (ptr) + (size_t)(h) * hstep, voffA); } } while (0)
; #define PG8_LDA(dst, b, h) do { _Pragma("unroll") for (int m = 0; m < 4; ++m) _Pragma("unroll") for (int k = 0; k < 2; ++k) dst[m][k] = *(const PG8_LAS bf16x8*)(lds + PG8_SA(b, h) + aoff + m * 2048 + k * 1024); } while (0)
; #define PG8_LDB(dst, b, h) do { _Pragma("unroll") for (int n = 0; n < 2; ++n) _Pragma("unroll") for (int k = 0; k < 2; ++k) dst[n][k] = *(const PG8_LAS bf16x8*)(lds + PG8_SB(b, h) + boff + n * 2048 + k * 1024); } while (0)
; #define PG8_WAIT_V(n) asm volatile("s_waitcnt vmcnt(" #n ")" ::: "memory")
; #define PG8_WAIT_L(n) asm volatile("s_waitcnt lgkmcnt(" #n ")" ::: "memory")
; #define PG8_BAR __builtin_amdgcn_s_barrier()
; #define PG8_SCHED __builtin_amdgcn_sched_barrier(0)
; template <class Epi, class Sched, bool ALIGN_EPI = false, bool SP2 = false, bool GATHER = false, bool FP8 = false>
; __device__ __forceinline__ void gemm_phase(PG8_LAS unsigned char* lds, const Gemm g, const Sched& S, const Epi& E, int tid_in  , const PG8_LAS unsigned* gofs = nullptr) {
;     ...
;             PG8_WAIT_V(8); PG8_WAIT_L(0); PG8_BAR; PG8_MMA(1, 0, At, B0); PG8_MMA(1, 1, At, B1); PG8_BAR; PG8_SCHED;
;             PG8_LDB(B0, 1, 0); PG8_LDB(B1, 1, 1); PG8_SCHED; PG8_LDA(At, 1, 0); PG8_STAGE_A(PG8_SA(0, 1), a2, 1, last);
;             PG8_WAIT_V(8); PG8_WAIT_L(0); PG8_BAR; PG8_MMA(0, 0, At, B0); PG8_MMA(0, 1, At, B1); PG8_BAR; PG8_SCHED;
	s_setprio 1
	s_waitcnt lgkmcnt(0)
	v_mfma_f32_16x16x32_bf16 v[64:67], v[132:135], v[164:167], v[64:67]
	v_mfma_f32_16x16x32_bf16 v[60:63], v[140:143], v[164:167], v[60:63]
	v_mfma_f32_16x16x32_bf16 v[48:51], v[132:135], v[172:175], v[48:51]
	v_mfma_f32_16x16x32_bf16 v[44:47], v[140:143], v[172:175], v[44:47]
	v_mfma_f32_16x16x32_bf16 v[32:35], v[132:135], v[190:193], v[32:35]
	v_mfma_f32_16x16x32_bf16 v[28:31], v[140:143], v[190:193], v[28:31]
	v_mfma_f32_16x16x32_bf16 v[16:19], v[132:135], v[198:201], v[16:19]
	v_mfma_f32_16x16x32_bf16 v[12:15], v[140:143], v[198:201], v[12:15]
	v_mfma_f32_16x16x32_bf16 v[64:67], v[136:139], v[168:171], v[64:67]
	v_mfma_f32_16x16x32_bf16 v[60:63], v[144:147], v[168:171], v[60:63]
	v_mfma_f32_16x16x32_bf16 v[48:51], v[136:139], v[176:179], v[48:51]
	v_mfma_f32_16x16x32_bf16 v[44:47], v[144:147], v[176:179], v[44:47]
	v_mfma_f32_16x16x32_bf16 v[32:35], v[136:139], v[194:197], v[32:35]
	v_mfma_f32_16x16x32_bf16 v[28:31], v[144:147], v[194:197], v[28:31]
	v_mfma_f32_16x16x32_bf16 v[16:19], v[136:139], v[202:205], v[16:19]
	v_mfma_f32_16x16x32_bf16 v[12:15], v[144:147], v[202:205], v[12:15]
	s_setprio 0
	s_setprio 1
	v_mfma_f32_16x16x32_bf16 v[56:59], v[148:151], v[164:167], v[56:59]
	v_mfma_f32_16x16x32_bf16 v[52:55], v[156:159], v[164:167], v[52:55]
	v_mfma_f32_16x16x32_bf16 v[40:43], v[148:151], v[172:175], v[40:43]
	v_mfma_f32_16x16x32_bf16 v[36:39], v[156:159], v[172:175], v[36:39]
	v_mfma_f32_16x16x32_bf16 v[24:27], v[148:151], v[190:193], v[24:27]
	v_mfma_f32_16x16x32_bf16 v[20:23], v[156:159], v[190:193], v[20:23]
	v_mfma_f32_16x16x32_bf16 v[8:11], v[148:151], v[198:201], v[8:11]
	v_mfma_f32_16x16x32_bf16 v[4:7], v[156:159], v[198:201], v[4:7]
	v_mfma_f32_16x16x32_bf16 v[56:59], v[152:155], v[168:171], v[56:59]
	v_mfma_f32_16x16x32_bf16 v[52:55], v[160:163], v[168:171], v[52:55]
	v_mfma_f32_16x16x32_bf16 v[40:43], v[152:155], v[176:179], v[40:43]
	v_mfma_f32_16x16x32_bf16 v[36:39], v[160:163], v[176:179], v[36:39]
	v_mfma_f32_16x16x32_bf16 v[24:27], v[152:155], v[194:197], v[24:27]
	v_mfma_f32_16x16x32_bf16 v[20:23], v[160:163], v[194:197], v[20:23]
	v_mfma_f32_16x16x32_bf16 v[8:11], v[152:155], v[202:205], v[8:11]
	v_mfma_f32_16x16x32_bf16 v[4:7], v[160:163], v[202:205], v[4:7]
	s_setprio 0
	s_barrier
	s_add_i32 s73, 0, 0x18000
	s_add_i32 s74, 0, 0x1c000
	v_add_u32_e32 v144, s73, v209
	v_add_u32_e32 v160, s74, v209
	ds_read_b128 v[132:135], v144
	ds_read_b128 v[136:139], v144 offset:1024
	ds_read_b128 v[140:143], v144 offset:2048
	ds_read_b128 v[144:147], v144 offset:3072
	ds_read_b128 v[148:151], v160
	ds_read_b128 v[152:155], v160 offset:1024
	ds_read_b128 v[156:159], v160 offset:2048
	ds_read_b128 v[160:163], v160 offset:3072
	s_add_u32 s44, s44, s24
	s_addc_u32 s45, s45, s25
	s_mov_b32 m0, s58
	v_lshl_add_u64 v[232:233], s[44:45], 0, v[0:1]
	ds_read_b128 v[164:167], v219 offset:32768
	ds_read_b128 v[168:171], v219 offset:33792
	ds_read_b128 v[172:175], v219 offset:34816
	ds_read_b128 v[176:179], v219 offset:35840
	ds_read_b128 v[190:193], v219 offset:36864
	ds_read_b128 v[194:197], v219 offset:37888
	ds_read_b128 v[198:201], v219 offset:38912
	ds_read_b128 v[202:205], v219 offset:39936
	global_load_lds_dwordx4 v[232:233], off
	v_lshl_add_u64 v[232:233], s[44:45], 0, v[182:183]
	s_mov_b32 m0, s59
	s_nop 0
	global_load_lds_dwordx4 v[232:233], off
	s_waitcnt vmcnt(8)
	s_waitcnt lgkmcnt(0)
	s_barrier
	s_setprio 1
	s_waitcnt lgkmcnt(0)
	v_mfma_f32_16x16x32_bf16 v[124:127], v[132:135], v[164:167], v[124:127]
	v_mfma_f32_16x16x32_bf16 v[128:131], v[140:143], v[164:167], v[128:131]
	v_mfma_f32_16x16x32_bf16 v[112:115], v[132:135], v[172:175], v[112:115]
	v_mfma_f32_16x16x32_bf16 v[108:111], v[140:143], v[172:175], v[108:111]
	v_mfma_f32_16x16x32_bf16 v[96:99], v[132:135], v[190:193], v[96:99]
	v_mfma_f32_16x16x32_bf16 v[92:95], v[140:143], v[190:193], v[92:95]
	v_mfma_f32_16x16x32_bf16 v[80:83], v[132:135], v[198:201], v[80:83]
	v_mfma_f32_16x16x32_bf16 v[76:79], v[140:143], v[198:201], v[76:79]
	v_mfma_f32_16x16x32_bf16 v[124:127], v[136:139], v[168:171], v[124:127]
	v_mfma_f32_16x16x32_bf16 v[128:131], v[144:147], v[168:171], v[128:131]
	v_mfma_f32_16x16x32_bf16 v[112:115], v[136:139], v[176:179], v[112:115]
	v_mfma_f32_16x16x32_bf16 v[108:111], v[144:147], v[176:179], v[108:111]
	v_mfma_f32_16x16x32_bf16 v[96:99], v[136:139], v[194:197], v[96:99]
	v_mfma_f32_16x16x32_bf16 v[92:95], v[144:147], v[194:197], v[92:95]
	v_mfma_f32_16x16x32_bf16 v[80:83], v[136:139], v[202:205], v[80:83]
	v_mfma_f32_16x16x32_bf16 v[76:79], v[144:147], v[202:205], v[76:79]
	s_setprio 0
	s_setprio 1
	v_mfma_f32_16x16x32_bf16 v[120:123], v[148:151], v[164:167], v[120:123]
	v_mfma_f32_16x16x32_bf16 v[116:119], v[156:159], v[164:167], v[116:119]
	v_mfma_f32_16x16x32_bf16 v[104:107], v[148:151], v[172:175], v[104:107]
	v_mfma_f32_16x16x32_bf16 v[100:103], v[156:159], v[172:175], v[100:103]
	v_mfma_f32_16x16x32_bf16 v[88:91], v[148:151], v[190:193], v[88:91]
	v_mfma_f32_16x16x32_bf16 v[84:87], v[156:159], v[190:193], v[84:87]
	v_mfma_f32_16x16x32_bf16 v[72:75], v[148:151], v[198:201], v[72:75]
	v_mfma_f32_16x16x32_bf16 v[68:71], v[156:159], v[198:201], v[68:71]
	v_mfma_f32_16x16x32_bf16 v[120:123], v[152:155], v[168:171], v[120:123]
	v_mfma_f32_16x16x32_bf16 v[116:119], v[160:163], v[168:171], v[116:119]
	v_mfma_f32_16x16x32_bf16 v[104:107], v[152:155], v[176:179], v[104:107]
	v_mfma_f32_16x16x32_bf16 v[100:103], v[160:163], v[176:179], v[100:103]
	v_mfma_f32_16x16x32_bf16 v[88:91], v[152:155], v[194:197], v[88:91]
	v_mfma_f32_16x16x32_bf16 v[84:87], v[160:163], v[194:197], v[84:87]
	v_mfma_f32_16x16x32_bf16 v[72:75], v[152:155], v[202:205], v[72:75]
	v_mfma_f32_16x16x32_bf16 v[68:71], v[160:163], v[202:205], v[68:71]
	s_setprio 0
	s_barrier
; #define PG8_STAGE(bufoff, gbase, voff) do { _Pragma("unroll") for (int _i = 0; _i < 2; ++_i) \
;         __builtin_amdgcn_global_load_lds((const unsigned*)((const char*)(gbase) + (voff)[_i]), (PG8_LAS unsigned*)(lds + (bufoff) + ldsw + _i * 8192), 16, 0, 0); } while (0)
; #define PG8_STAGE_A(bufoff, ptr, h, nx) do { if constexpr (GATHER) { const int ub_ = ((nx) ? gnext : ui) * 256 + (h) * 128; unsigned vv_[2]; _Pragma("unroll") for (int _j = 0; _j < 2; ++_j) vv_[_j] = gofs[ub_ + gL[_j]] + (unsigned)gC[_j]; PG8_STAGE(bufoff, ptr, vv_); } \
;         else { PG8_STAGE(bufoff, (ptr) + (size_t)(h) * hstep, voffA); } } while (0)
; #define PG8_LDA(dst, b, h) do { _Pragma("unroll") for (int m = 0; m < 4; ++m) _Pragma("unroll") for (int k = 0; k < 2; ++k) dst[m][k] = *(const PG8_LAS bf16x8*)(lds + PG8_SA(b, h) + aoff + m * 2048 + k * 1024); } while (0)
; #define PG8_WAIT_V(n) asm volatile("s_waitcnt vmcnt(" #n ")" ::: "memory")
; #define PG8_WAIT_L(n) asm volatile("s_waitcnt lgkmcnt(" #n ")" ::: "memory")
; #define PG8_BAR __builtin_amdgcn_s_barrier()
; #define PG8_SCHED __builtin_amdgcn_sched_barrier(0)
; template <class Epi, class Sched, bool ALIGN_EPI = false, bool SP2 = false, bool GATHER = false, bool FP8 = false>
; __device__ __forceinline__ void gemm_phase(PG8_LAS unsigned char* lds, const Gemm g, const Sched& S, const Epi& E, int tid_in  , const PG8_LAS unsigned* gofs = nullptr) {
;     ...
;         for (int t = 0; t < nt; t += 2) {
;             const bool last = (t == nt - 2);
;             const char* a1 = cA + (size_t)(t + 1) * kstep;
;             const char* a2 = last ? nA : cA + (size_t)(t + 2) * kstep; const char* b2 = last ? nB : cB + (size_t)(t + 2) * kstep;
;             const char* a3 = a2 + kstep; const char* b3 = b2 + kstep;
;     ...
;             PG8_LDA(At, 1, 1); PG8_STAGE(PG8_SB(1, 0), b3, voffB); PG8_STAGE(PG8_SB(1, 1), b3 + hstep, voffB); PG8_STAGE_A(PG8_SA(1, 0), a3, 0, last);
;             PG8_WAIT_V(8); PG8_WAIT_L(0); PG8_BAR; PG8_MMA(1, 0, At, B0); PG8_MMA(1, 1, At, B1); PG8_BAR; PG8_SCHED;
	s_add_i32 s44, s73, s46
	v_lshl_add_u64 v[220:221], v[220:221], 0, s[38:39]
	s_mov_b32 m0, s44
	ds_read_b128 v[164:167], v219 offset:49152
	ds_read_b128 v[168:171], v219 offset:50176
	ds_read_b128 v[172:175], v219 offset:51200
	ds_read_b128 v[176:179], v219 offset:52224
	ds_read_b128 v[190:193], v219 offset:53248
	ds_read_b128 v[194:197], v219 offset:54272
	ds_read_b128 v[198:201], v219 offset:55296
	ds_read_b128 v[202:205], v219 offset:56320
	global_load_lds_dwordx4 v[220:221], off
	v_lshl_add_u64 v[220:221], v[222:223], 0, s[38:39]
	s_add_i32 m0, s44, 0x2000
	s_add_i32 s44, s74, s46
	global_load_lds_dwordx4 v[220:221], off
	v_lshl_add_u64 v[220:221], v[224:225], 0, s[38:39]
	s_mov_b32 m0, s44
	s_nop 0
	global_load_lds_dwordx4 v[220:221], off
	v_lshl_add_u64 v[220:221], v[226:227], 0, s[38:39]
	s_add_i32 m0, s44, 0x2000
	s_nop 0
	global_load_lds_dwordx4 v[220:221], off
	v_lshl_add_u64 v[220:221], v[228:229], 0, s[38:39]
	s_mov_b32 m0, s62
	s_nop 0
	global_load_lds_dwordx4 v[220:221], off
	v_lshl_add_u64 v[220:221], v[230:231], 0, s[38:39]
	s_mov_b32 m0, s63
	s_nop 0
	global_load_lds_dwordx4 v[220:221], off
	s_waitcnt vmcnt(8)
	s_waitcnt lgkmcnt(0)
	s_barrier
	s_setprio 1
	s_waitcnt lgkmcnt(0)
	v_mfma_f32_16x16x32_bf16 v[64:67], v[132:135], v[164:167], v[64:67]
	s_add_u32 s42, s42, 0x100
	v_mfma_f32_16x16x32_bf16 v[60:63], v[140:143], v[164:167], v[60:63]
	s_addc_u32 s43, s43, 0
	v_mfma_f32_16x16x32_bf16 v[48:51], v[132:135], v[172:175], v[48:51]
	s_add_u32 s70, s70, 0x100
	v_mfma_f32_16x16x32_bf16 v[44:47], v[140:143], v[172:175], v[44:47]
	s_addc_u32 s71, s71, 0
	v_mfma_f32_16x16x32_bf16 v[32:35], v[132:135], v[190:193], v[32:35]
	s_cmp_ge_i32 s72, s61
	v_mfma_f32_16x16x32_bf16 v[28:31], v[140:143], v[190:193], v[28:31]
	s_cselect_b32 vcc_lo, 1, 0
	v_mfma_f32_16x16x32_bf16 v[16:19], v[132:135], v[198:201], v[16:19]
	s_mov_b32 s44, s72
	v_mfma_f32_16x16x32_bf16 v[12:15], v[140:143], v[198:201], v[12:15]
	s_add_i32 s72, s44, 2
	v_mfma_f32_16x16x32_bf16 v[64:67], v[136:139], v[168:171], v[64:67]
	s_add_u32 s73, s42, 0x80
	v_mfma_f32_16x16x32_bf16 v[60:63], v[144:147], v[168:171], v[60:63]
	s_addc_u32 s45, s43, 0
	v_mfma_f32_16x16x32_bf16 v[48:51], v[136:139], v[176:179], v[48:51]
	s_add_i32 s76, 0, 0x10000
	v_mfma_f32_16x16x32_bf16 v[44:47], v[144:147], v[176:179], v[44:47]
	s_cmp_eq_u32 s64, s44
	v_mfma_f32_16x16x32_bf16 v[32:35], v[136:139], v[194:197], v[32:35]
	s_cselect_b32 s45, s7, s45
	v_mfma_f32_16x16x32_bf16 v[28:31], v[144:147], v[194:197], v[28:31]
	s_cselect_b32 s44, s6, s73
	v_mfma_f32_16x16x32_bf16 v[16:19], v[136:139], v[202:205], v[16:19]
	s_cselect_b32 s75, s41, s71
	v_mfma_f32_16x16x32_bf16 v[12:15], v[144:147], v[202:205], v[12:15]
	s_cselect_b32 s74, s40, s70
	s_setprio 0
	s_setprio 1
	v_mfma_f32_16x16x32_bf16 v[56:59], v[148:151], v[164:167], v[56:59]
	s_add_i32 s73, 0, 0x14000
	v_mfma_f32_16x16x32_bf16 v[52:55], v[156:159], v[164:167], v[52:55]
	v_mfma_f32_16x16x32_bf16 v[40:43], v[148:151], v[172:175], v[40:43]
	v_mfma_f32_16x16x32_bf16 v[36:39], v[156:159], v[172:175], v[36:39]
	v_mfma_f32_16x16x32_bf16 v[24:27], v[148:151], v[190:193], v[24:27]
	v_mfma_f32_16x16x32_bf16 v[20:23], v[156:159], v[190:193], v[20:23]
	v_mfma_f32_16x16x32_bf16 v[8:11], v[148:151], v[198:201], v[8:11]
	v_mfma_f32_16x16x32_bf16 v[4:7], v[156:159], v[198:201], v[4:7]
	v_mfma_f32_16x16x32_bf16 v[56:59], v[152:155], v[168:171], v[56:59]
	v_mfma_f32_16x16x32_bf16 v[52:55], v[160:163], v[168:171], v[52:55]
	v_mfma_f32_16x16x32_bf16 v[40:43], v[152:155], v[176:179], v[40:43]
	v_mfma_f32_16x16x32_bf16 v[36:39], v[160:163], v[176:179], v[36:39]
	v_mfma_f32_16x16x32_bf16 v[24:27], v[152:155], v[194:197], v[24:27]
	v_mfma_f32_16x16x32_bf16 v[20:23], v[160:163], v[194:197], v[20:23]
	v_mfma_f32_16x16x32_bf16 v[8:11], v[152:155], v[202:205], v[8:11]
	v_mfma_f32_16x16x32_bf16 v[4:7], v[160:163], v[202:205], v[4:7]
	s_setprio 0
	s_barrier
	s_cmp_eq_u32 vcc_lo, 0
	s_cbranch_scc1 .Lkrot4_body

; #define PG8_STAGE(bufoff, gbase, voff) do { _Pragma("unroll") for (int _i = 0; _i < 2; ++_i) \
;         __builtin_amdgcn_global_load_lds((const unsigned*)((const char*)(gbase) + (voff)[_i]), (PG8_LAS unsigned*)(lds + (bufoff) + ldsw + _i * 8192), 16, 0, 0); } while (0)
; #define PG8_STAGE_A(bufoff, ptr, h, nx) do { if constexpr (GATHER) { const int ub_ = ((nx) ? gnext : ui) * 256 + (h) * 128; unsigned vv_[2]; _Pragma("unroll") for (int _j = 0; _j < 2; ++_j) vv_[_j] = gofs[ub_ + gL[_j]] + (unsigned)gC[_j]; PG8_STAGE(bufoff, ptr, vv_); } \
;         else { PG8_STAGE(bufoff, (ptr) + (size_t)(h) * hstep, voffA); } } while (0)
; #define PG8_LDA(dst, b, h) do { _Pragma("unroll") for (int m = 0; m < 4; ++m) _Pragma("unroll") for (int k = 0; k < 2; ++k) dst[m][k] = *(const PG8_LAS bf16x8*)(lds + PG8_SA(b, h) + aoff + m * 2048 + k * 1024); } while (0)
; #define PG8_LDB(dst, b, h) do { _Pragma("unroll") for (int n = 0; n < 2; ++n) _Pragma("unroll") for (int k = 0; k < 2; ++k) dst[n][k] = *(const PG8_LAS bf16x8*)(lds + PG8_SB(b, h) + boff + n * 2048 + k * 1024); } while (0)
; #define PG8_WAIT_V(n) asm volatile("s_waitcnt vmcnt(" #n ")" ::: "memory")
; #define PG8_WAIT_L(n) asm volatile("s_waitcnt lgkmcnt(" #n ")" ::: "memory")
; #define PG8_BAR __builtin_amdgcn_s_barrier()
; #define PG8_SCHED __builtin_amdgcn_sched_barrier(0)
; template <class Epi, class Sched, bool ALIGN_EPI = false, bool SP2 = false, bool GATHER = false, bool FP8 = false>
; __device__ __forceinline__ void gemm_phase(PG8_LAS unsigned char* lds, const Gemm g, const Sched& S, const Epi& E, int tid_in  , const PG8_LAS unsigned* gofs = nullptr) {
;     ...
;             PG8_LDB(B0, 0, 0); PG8_LDB(B1, 0, 1); PG8_SCHED; PG8_LDA(At, 0, 0); PG8_STAGE_A(PG8_SA(1, 1), a1, 1, false);
;             PG8_WAIT_V(8); PG8_WAIT_L(0); PG8_BAR; PG8_MMA(0, 0, At, B0); PG8_MMA(0, 1, At, B1); PG8_BAR; PG8_SCHED;
;             PG8_LDA(At, 0, 1); PG8_STAGE(PG8_SB(0, 0), b2, voffB); PG8_STAGE(PG8_SB(0, 1), b2 + hstep, voffB); PG8_STAGE_A(PG8_SA(0, 0), a2, 0, last);
;             PG8_WAIT_V(8); PG8_WAIT_L(0); PG8_BAR; PG8_MMA(1, 0, At, B0); PG8_MMA(1, 1, At, B1); PG8_BAR; PG8_SCHED;
;             PG8_LDB(B0, 1, 0); PG8_LDB(B1, 1, 1); PG8_SCHED; PG8_LDA(At, 1, 0); PG8_STAGE_A(PG8_SA(0, 1), a2, 1, last);
;             PG8_WAIT_V(8); PG8_WAIT_L(0); PG8_BAR; PG8_MMA(0, 0, At, B0); PG8_MMA(0, 1, At, B1); PG8_BAR; PG8_SCHED;
.Lkrot5_body:
	v_add_u32_e32 v4, s54, v186
	v_add_u32_e32 v8, s55, v186
	ds_read_b128 v[28:31], v4
	ds_read_b128 v[32:35], v4 offset:1024
	ds_read_b128 v[20:23], v4 offset:2048
	ds_read_b128 v[24:27], v4 offset:3072
	ds_read_b128 v[12:15], v8
	ds_read_b128 v[16:19], v8 offset:1024
	ds_read_b128 v[4:7], v8 offset:2048
	ds_read_b128 v[8:11], v8 offset:3072
	v_lshl_add_u64 v[182:183], s[20:21], 0, v[170:171]
	s_add_i32 m0, s36, 0xc000
	ds_read_b128 v[174:177], v208
	ds_read_b128 v[178:181], v208 offset:1024
	ds_read_b128 v[218:221], v208 offset:2048
	ds_read_b128 v[222:225], v208 offset:3072
	ds_read_b128 v[226:229], v208 offset:4096
	ds_read_b128 v[230:233], v208 offset:5120
	ds_read_b128 v[234:237], v208 offset:6144
	ds_read_b128 v[238:241], v208 offset:7168
	global_load_lds_dwordx4 v[182:183], off
	v_lshl_add_u64 v[182:183], s[20:21], 0, v[172:173]
	s_add_i32 m0, s36, 0xe000
	s_nop 0
	global_load_lds_dwordx4 v[182:183], off
	s_waitcnt vmcnt(8)
	s_waitcnt lgkmcnt(0)
	s_barrier
	s_setprio 1
	s_waitcnt lgkmcnt(0)
	v_mfma_f32_16x16x128_f8f6f4 v[160:163], v[28:35], v[174:181], v[160:163]
	v_mfma_f32_16x16x128_f8f6f4 v[156:159], v[20:27], v[174:181], v[156:159]
	v_mfma_f32_16x16x128_f8f6f4 v[152:155], v[28:35], v[218:225], v[152:155]
	v_mfma_f32_16x16x128_f8f6f4 v[148:151], v[20:27], v[218:225], v[148:151]
	v_mfma_f32_16x16x128_f8f6f4 v[140:143], v[28:35], v[226:233], v[140:143]
	v_mfma_f32_16x16x128_f8f6f4 v[132:135], v[20:27], v[226:233], v[132:135]
	v_mfma_f32_16x16x128_f8f6f4 v[124:127], v[28:35], v[234:241], v[124:127]
	v_mfma_f32_16x16x128_f8f6f4 v[116:119], v[20:27], v[234:241], v[116:119]
	s_setprio 0
	s_setprio 1
	v_mfma_f32_16x16x128_f8f6f4 v[144:147], v[12:19], v[174:181], v[144:147]
	v_mfma_f32_16x16x128_f8f6f4 v[136:139], v[4:11], v[174:181], v[136:139]
	v_mfma_f32_16x16x128_f8f6f4 v[128:131], v[12:19], v[218:225], v[128:131]
	v_mfma_f32_16x16x128_f8f6f4 v[120:123], v[4:11], v[218:225], v[120:123]
	v_mfma_f32_16x16x128_f8f6f4 v[112:115], v[12:19], v[226:233], v[112:115]
	v_mfma_f32_16x16x128_f8f6f4 v[108:111], v[4:11], v[226:233], v[108:111]
	v_mfma_f32_16x16x128_f8f6f4 v[104:107], v[12:19], v[234:241], v[104:107]
	v_mfma_f32_16x16x128_f8f6f4 v[100:103], v[4:11], v[234:241], v[100:103]
	s_setprio 0
	s_barrier
	s_add_i32 s54, s54, s30
	v_lshl_add_u64 v[174:175], s[24:25], 0, v[164:165]
	s_mov_b32 m0, s54
	ds_read_b128 v[218:221], v208 offset:16384
	ds_read_b128 v[222:225], v208 offset:17408
	ds_read_b128 v[226:229], v208 offset:18432
	ds_read_b128 v[230:233], v208 offset:19456
	ds_read_b128 v[234:237], v208 offset:20480
	ds_read_b128 v[238:241], v208 offset:21504
	ds_read_b128 v[242:245], v208 offset:22528
	ds_read_b128 v[246:249], v208 offset:23552
	global_load_lds_dwordx4 v[174:175], off
	s_add_i32 m0, s54, 0x2000
	v_lshl_add_u64 v[176:177], s[24:25], 0, v[168:169]
	s_add_u32 s24, s24, s0
	s_addc_u32 s25, s25, s1
	s_add_i32 s54, s55, s30
	global_load_lds_dwordx4 v[176:177], off
	v_lshl_add_u64 v[178:179], s[24:25], 0, v[164:165]
	s_mov_b32 m0, s54
	v_lshl_add_u64 v[180:181], s[24:25], 0, v[168:169]
	global_load_lds_dwordx4 v[178:179], off
	s_add_i32 m0, s54, 0x2000
	v_lshl_add_u64 v[182:183], s[22:23], 0, v[0:1]
	global_load_lds_dwordx4 v[180:181], off
	s_mov_b32 m0, s36
	v_lshl_add_u64 v[184:185], s[22:23], 0, v[166:167]
	global_load_lds_dwordx4 v[182:183], off
	s_mov_b32 m0, s37
	s_nop 0
	global_load_lds_dwordx4 v[184:185], off
	s_waitcnt vmcnt(8)
	s_waitcnt lgkmcnt(0)
	s_barrier
	s_setprio 1
	s_waitcnt lgkmcnt(0)
	v_mfma_f32_16x16x128_f8f6f4 v[96:99], v[28:35], v[218:225], v[96:99]
	v_mfma_f32_16x16x128_f8f6f4 v[92:95], v[20:27], v[218:225], v[92:95]
	v_mfma_f32_16x16x128_f8f6f4 v[88:91], v[28:35], v[226:233], v[88:91]
	v_mfma_f32_16x16x128_f8f6f4 v[84:87], v[20:27], v[226:233], v[84:87]
	v_mfma_f32_16x16x128_f8f6f4 v[76:79], v[28:35], v[234:241], v[76:79]
	v_mfma_f32_16x16x128_f8f6f4 v[68:71], v[20:27], v[234:241], v[68:71]
	v_mfma_f32_16x16x128_f8f6f4 v[60:63], v[28:35], v[242:249], v[60:63]
	v_mfma_f32_16x16x128_f8f6f4 v[52:55], v[20:27], v[242:249], v[52:55]
	s_setprio 0
	s_setprio 1
	v_mfma_f32_16x16x128_f8f6f4 v[80:83], v[12:19], v[218:225], v[80:83]
	v_mfma_f32_16x16x128_f8f6f4 v[72:75], v[4:11], v[218:225], v[72:75]
	v_mfma_f32_16x16x128_f8f6f4 v[64:67], v[12:19], v[226:233], v[64:67]
	v_mfma_f32_16x16x128_f8f6f4 v[56:59], v[4:11], v[226:233], v[56:59]
	v_mfma_f32_16x16x128_f8f6f4 v[48:51], v[12:19], v[234:241], v[48:51]
	v_mfma_f32_16x16x128_f8f6f4 v[44:47], v[4:11], v[234:241], v[44:47]
	v_mfma_f32_16x16x128_f8f6f4 v[40:43], v[12:19], v[242:249], v[40:43]
	v_mfma_f32_16x16x128_f8f6f4 v[36:39], v[4:11], v[242:249], v[36:39]
	s_setprio 0
	s_barrier
	s_add_i32 s24, 0, 0x18000
	s_add_i32 s25, 0, 0x1c000
	v_add_u32_e32 v16, s24, v186
	v_add_u32_e32 v32, s25, v186
	ds_read_b128 v[4:7], v16
	ds_read_b128 v[8:11], v16 offset:1024
	ds_read_b128 v[12:15], v16 offset:2048
	ds_read_b128 v[16:19], v16 offset:3072
	ds_read_b128 v[20:23], v32
	ds_read_b128 v[24:27], v32 offset:1024
	ds_read_b128 v[28:31], v32 offset:2048
	ds_read_b128 v[32:35], v32 offset:3072
	s_add_u32 s22, s22, s0
	s_addc_u32 s23, s23, s1
	s_mov_b32 m0, s40
	v_lshl_add_u64 v[198:199], s[22:23], 0, v[0:1]
	ds_read_b128 v[218:221], v208 offset:32768
	ds_read_b128 v[222:225], v208 offset:33792
	ds_read_b128 v[226:229], v208 offset:34816
	ds_read_b128 v[230:233], v208 offset:35840
	ds_read_b128 v[234:237], v208 offset:36864
	ds_read_b128 v[238:241], v208 offset:37888
	ds_read_b128 v[242:245], v208 offset:38912
	ds_read_b128 v[246:249], v208 offset:39936
	global_load_lds_dwordx4 v[198:199], off
	v_lshl_add_u64 v[198:199], s[22:23], 0, v[166:167]
	s_mov_b32 m0, s41
	s_nop 0
	global_load_lds_dwordx4 v[198:199], off
	s_waitcnt vmcnt(8)
	s_waitcnt lgkmcnt(0)
	s_barrier
; #define PG8_STAGE(bufoff, gbase, voff) do { _Pragma("unroll") for (int _i = 0; _i < 2; ++_i) \
;         __builtin_amdgcn_global_load_lds((const unsigned*)((const char*)(gbase) + (voff)[_i]), (PG8_LAS unsigned*)(lds + (bufoff) + ldsw + _i * 8192), 16, 0, 0); } while (0)
; #define PG8_STAGE_A(bufoff, ptr, h, nx) do { if constexpr (GATHER) { const int ub_ = ((nx) ? gnext : ui) * 256 + (h) * 128; unsigned vv_[2]; _Pragma("unroll") for (int _j = 0; _j < 2; ++_j) vv_[_j] = gofs[ub_ + gL[_j]] + (unsigned)gC[_j]; PG8_STAGE(bufoff, ptr, vv_); } \
;         else { PG8_STAGE(bufoff, (ptr) + (size_t)(h) * hstep, voffA); } } while (0)
; #define PG8_LDA(dst, b, h) do { _Pragma("unroll") for (int m = 0; m < 4; ++m) _Pragma("unroll") for (int k = 0; k < 2; ++k) dst[m][k] = *(const PG8_LAS bf16x8*)(lds + PG8_SA(b, h) + aoff + m * 2048 + k * 1024); } while (0)
; #define PG8_WAIT_V(n) asm volatile("s_waitcnt vmcnt(" #n ")" ::: "memory")
; #define PG8_WAIT_L(n) asm volatile("s_waitcnt lgkmcnt(" #n ")" ::: "memory")
; #define PG8_BAR __builtin_amdgcn_s_barrier()
; #define PG8_SCHED __builtin_amdgcn_sched_barrier(0)
; template <class Epi, class Sched, bool ALIGN_EPI = false, bool SP2 = false, bool GATHER = false, bool FP8 = false>
; __device__ __forceinline__ void gemm_phase(PG8_LAS unsigned char* lds, const Gemm g, const Sched& S, const Epi& E, int tid_in  , const PG8_LAS unsigned* gofs = nullptr) {
;     ...
;         for (int t = 0; t < nt; t += 2) {
;             const bool last = (t == nt - 2);
;             const char* a1 = cA + (size_t)(t + 1) * kstep;
;             const char* a2 = last ? nA : cA + (size_t)(t + 2) * kstep; const char* b2 = last ? nB : cB + (size_t)(t + 2) * kstep;
;             const char* a3 = a2 + kstep; const char* b3 = b2 + kstep;
;             if (last && has_next) S.a_ready(nxt);
;     ...
;             PG8_WAIT_V(8); PG8_WAIT_L(0); PG8_BAR; PG8_MMA(0, 0, At, B0); PG8_MMA(0, 1, At, B1); PG8_BAR; PG8_SCHED;
;             PG8_LDA(At, 1, 1); PG8_STAGE(PG8_SB(1, 0), b3, voffB); PG8_STAGE(PG8_SB(1, 1), b3 + hstep, voffB); PG8_STAGE_A(PG8_SA(1, 0), a3, 0, last);
;             PG8_WAIT_V(8); PG8_WAIT_L(0); PG8_BAR; PG8_MMA(1, 0, At, B0); PG8_MMA(1, 1, At, B1); PG8_BAR; PG8_SCHED;
	s_setprio 1
	s_waitcnt lgkmcnt(0)
	v_mfma_f32_16x16x128_f8f6f4 v[160:163], v[4:11], v[218:225], v[160:163]
	v_mfma_f32_16x16x128_f8f6f4 v[156:159], v[12:19], v[218:225], v[156:159]
	v_mfma_f32_16x16x128_f8f6f4 v[152:155], v[4:11], v[226:233], v[152:155]
	v_mfma_f32_16x16x128_f8f6f4 v[148:151], v[12:19], v[226:233], v[148:151]
	v_mfma_f32_16x16x128_f8f6f4 v[140:143], v[4:11], v[234:241], v[140:143]
	v_mfma_f32_16x16x128_f8f6f4 v[132:135], v[12:19], v[234:241], v[132:135]
	v_mfma_f32_16x16x128_f8f6f4 v[124:127], v[4:11], v[242:249], v[124:127]
	v_mfma_f32_16x16x128_f8f6f4 v[116:119], v[12:19], v[242:249], v[116:119]
	s_setprio 0
	s_setprio 1
	v_mfma_f32_16x16x128_f8f6f4 v[144:147], v[20:27], v[218:225], v[144:147]
	v_mfma_f32_16x16x128_f8f6f4 v[136:139], v[28:35], v[218:225], v[136:139]
	v_mfma_f32_16x16x128_f8f6f4 v[128:131], v[20:27], v[226:233], v[128:131]
	v_mfma_f32_16x16x128_f8f6f4 v[120:123], v[28:35], v[226:233], v[120:123]
	v_mfma_f32_16x16x128_f8f6f4 v[112:115], v[20:27], v[234:241], v[112:115]
	v_mfma_f32_16x16x128_f8f6f4 v[108:111], v[28:35], v[234:241], v[108:111]
	v_mfma_f32_16x16x128_f8f6f4 v[104:107], v[20:27], v[242:249], v[104:107]
	v_mfma_f32_16x16x128_f8f6f4 v[100:103], v[28:35], v[242:249], v[100:103]
	s_setprio 0
	s_barrier
	s_add_i32 s22, s24, s30
	v_lshl_add_u64 v[174:175], v[174:175], 0, s[38:39]
	s_mov_b32 m0, s22
	ds_read_b128 v[218:221], v208 offset:49152
	ds_read_b128 v[222:225], v208 offset:50176
	ds_read_b128 v[226:229], v208 offset:51200
	ds_read_b128 v[230:233], v208 offset:52224
	ds_read_b128 v[234:237], v208 offset:53248
	ds_read_b128 v[238:241], v208 offset:54272
	ds_read_b128 v[242:245], v208 offset:55296
	ds_read_b128 v[246:249], v208 offset:56320
	global_load_lds_dwordx4 v[174:175], off
	v_lshl_add_u64 v[174:175], v[176:177], 0, s[38:39]
	s_add_i32 m0, s22, 0x2000
	s_add_i32 s22, s25, s30
	global_load_lds_dwordx4 v[174:175], off
	v_lshl_add_u64 v[174:175], v[178:179], 0, s[38:39]
	s_mov_b32 m0, s22
	s_nop 0
	global_load_lds_dwordx4 v[174:175], off
	v_lshl_add_u64 v[174:175], v[180:181], 0, s[38:39]
	s_add_i32 m0, s22, 0x2000
	s_nop 0
	global_load_lds_dwordx4 v[174:175], off
	v_lshl_add_u64 v[174:175], v[182:183], 0, s[38:39]
	s_mov_b32 m0, s45
	s_nop 0
	global_load_lds_dwordx4 v[174:175], off
	v_lshl_add_u64 v[174:175], v[184:185], 0, s[38:39]
	s_mov_b32 m0, s46
	s_nop 0
	global_load_lds_dwordx4 v[174:175], off
	s_waitcnt vmcnt(8)
	s_waitcnt lgkmcnt(0)
	s_barrier
	s_setprio 1
	s_waitcnt lgkmcnt(0)
	v_mfma_f32_16x16x128_f8f6f4 v[96:99], v[4:11], v[218:225], v[96:99]
	s_add_u32 s20, s20, 0x100
	s_addc_u32 s21, s21, 0
	v_mfma_f32_16x16x128_f8f6f4 v[92:95], v[12:19], v[218:225], v[92:95]
	s_add_u32 s51, s51, 0x100
	s_addc_u32 s52, s52, 0
	v_mfma_f32_16x16x128_f8f6f4 v[88:91], v[4:11], v[226:233], v[88:91]
	s_cmp_ge_i32 s53, s42
	s_cselect_b32 vcc_lo, 1, 0
	v_mfma_f32_16x16x128_f8f6f4 v[84:87], v[12:19], v[226:233], v[84:87]
	s_mov_b32 s22, s53
	s_add_i32 s53, s22, 2
	v_mfma_f32_16x16x128_f8f6f4 v[76:79], v[4:11], v[234:241], v[76:79]
	s_add_u32 s24, s20, 0x80
	s_addc_u32 s23, s21, 0
	v_mfma_f32_16x16x128_f8f6f4 v[68:71], v[12:19], v[234:241], v[68:71]
	s_add_i32 s54, 0, 0x10000
	s_cmp_eq_u32 s47, s22
	v_mfma_f32_16x16x128_f8f6f4 v[60:63], v[4:11], v[242:249], v[60:63]
	s_cselect_b32 s23, s13, s23
	s_cselect_b32 s22, s12, s24
	v_mfma_f32_16x16x128_f8f6f4 v[52:55], v[12:19], v[242:249], v[52:55]
	s_cselect_b32 s25, s17, s52
	s_cselect_b32 s24, s16, s51
	s_setprio 0
	s_setprio 1
	v_mfma_f32_16x16x128_f8f6f4 v[80:83], v[20:27], v[218:225], v[80:83]
	s_add_i32 s55, 0, 0x14000
	v_mfma_f32_16x16x128_f8f6f4 v[72:75], v[28:35], v[218:225], v[72:75]
	v_mfma_f32_16x16x128_f8f6f4 v[64:67], v[20:27], v[226:233], v[64:67]
	v_mfma_f32_16x16x128_f8f6f4 v[56:59], v[28:35], v[226:233], v[56:59]
	v_mfma_f32_16x16x128_f8f6f4 v[48:51], v[20:27], v[234:241], v[48:51]
	v_mfma_f32_16x16x128_f8f6f4 v[44:47], v[28:35], v[234:241], v[44:47]
	v_mfma_f32_16x16x128_f8f6f4 v[40:43], v[20:27], v[242:249], v[40:43]
	v_mfma_f32_16x16x128_f8f6f4 v[36:39], v[28:35], v[242:249], v[36:39]
	s_setprio 0
	s_barrier
;     __device__ __forceinline__ void operator()(const f32x4 (&acc)[2][2][4][2], const Unit& u, int wr, int wc, int fr, int fq) const {
;     ...
;             for (int m = 0; m < 4; ++m) { const int rl = rl0 + ai * HALF + m * 16; if (rl < nv) {
;                 const f32x4 v00 = acc[ai][0][m][0] * sc, v01 = acc[ai][0][m][1] * sc, v10 = acc[ai][1][m][0] * sc, v11 = acc[ai][1][m][1] * sc;
;                 u32x4 w; w.x = pk4_fp8(v00[0], v00[1], v00[2], v00[3]); w.y = pk4_fp8(v01[0], v01[1], v01[2], v01[3]); w.z = pk4_fp8(v10[0], v10[1], v10[2], v10[3]); w.w = pk4_fp8(v11[0], v11[1], v11[2], v11[3]);
; template <class Epi, class Sched, bool ALIGN_EPI = false, bool SP2 = false, bool GATHER = false, bool FP8 = false>
; __device__ __forceinline__ void gemm_phase(PG8_LAS unsigned char* lds, const Gemm g, const Sched& S, const Epi& E, int tid_in  , const PG8_LAS unsigned* gofs = nullptr) {
;     ...
;         for (int t = 0; t < nt; t += 2) {
;             const bool last = (t == nt - 2);
;             const char* a1 = cA + (size_t)(t + 1) * kstep;
;             const char* a2 = last ? nA : cA + (size_t)(t + 2) * kstep; const char* b2 = last ? nB : cB + (size_t)(t + 2) * kstep;
	s_cmp_eq_u32 vcc_lo, 0
	s_cbranch_scc1 .Lkrot5_body
	s_mov_b32 s20, 0x3d800000
	v_pk_mul_f32 v[182:183], v[162:163], s[20:21] op_sel_hi:[1,0]
	v_pk_mul_f32 v[184:185], v[160:161], s[20:21] op_sel_hi:[1,0]
	v_pk_mul_f32 v[176:177], v[158:159], s[20:21] op_sel_hi:[1,0]
	v_pk_mul_f32 v[180:181], v[156:157], s[20:21] op_sel_hi:[1,0]
	v_pk_mul_f32 v[174:175], v[146:147], s[20:21] op_sel_hi:[1,0]
	v_pk_mul_f32 v[178:179], v[144:145], s[20:21] op_sel_hi:[1,0]
	v_pk_mul_f32 v[160:161], v[138:139], s[20:21] op_sel_hi:[1,0]
	v_pk_mul_f32 v[162:163], v[136:137], s[20:21] op_sel_hi:[1,0]
	v_pk_mul_f32 v[156:157], v[154:155], s[20:21] op_sel_hi:[1,0]
	v_pk_mul_f32 v[158:159], v[152:153], s[20:21] op_sel_hi:[1,0]
	v_pk_mul_f32 v[150:151], v[150:151], s[20:21] op_sel_hi:[1,0]
	v_pk_mul_f32 v[154:155], v[148:149], s[20:21] op_sel_hi:[1,0]
	v_pk_mul_f32 v[148:149], v[130:131], s[20:21] op_sel_hi:[1,0]
	v_pk_mul_f32 v[152:153], v[128:129], s[20:21] op_sel_hi:[1,0]
	v_pk_mul_f32 v[144:145], v[122:123], s[20:21] op_sel_hi:[1,0]
	v_pk_mul_f32 v[146:147], v[120:121], s[20:21] op_sel_hi:[1,0]
	v_pk_mul_f32 v[142:143], v[142:143], s[20:21] op_sel_hi:[1,0]
	v_pk_mul_f32 v[140:141], v[140:141], s[20:21] op_sel_hi:[1,0]
	v_pk_mul_f32 v[134:135], v[134:135], s[20:21] op_sel_hi:[1,0]
	v_pk_mul_f32 v[138:139], v[132:133], s[20:21] op_sel_hi:[1,0]
	v_pk_mul_f32 v[132:133], v[114:115], s[20:21] op_sel_hi:[1,0]
	v_pk_mul_f32 v[136:137], v[112:113], s[20:21] op_sel_hi:[1,0]
	v_pk_mul_f32 v[128:129], v[110:111], s[20:21] op_sel_hi:[1,0]
	v_pk_mul_f32 v[130:131], v[108:109], s[20:21] op_sel_hi:[1,0]
	v_pk_mul_f32 v[120:121], v[126:127], s[20:21] op_sel_hi:[1,0]
	v_pk_mul_f32 v[122:123], v[124:125], s[20:21] op_sel_hi:[1,0]
	v_pk_mul_f32 v[114:115], v[118:119], s[20:21] op_sel_hi:[1,0]
	v_pk_mul_f32 v[118:119], v[116:117], s[20:21] op_sel_hi:[1,0]
	v_pk_mul_f32 v[112:113], v[106:107], s[20:21] op_sel_hi:[1,0]
	v_pk_mul_f32 v[116:117], v[104:105], s[20:21] op_sel_hi:[1,0]
	v_pk_mul_f32 v[108:109], v[102:103], s[20:21] op_sel_hi:[1,0]
	v_pk_mul_f32 v[110:111], v[100:101], s[20:21] op_sel_hi:[1,0]
	v_pk_mul_f32 v[104:105], v[98:99], s[20:21] op_sel_hi:[1,0]
	v_pk_mul_f32 v[106:107], v[96:97], s[20:21] op_sel_hi:[1,0]
	v_pk_mul_f32 v[98:99], v[94:95], s[20:21] op_sel_hi:[1,0]
	v_pk_mul_f32 v[102:103], v[92:93], s[20:21] op_sel_hi:[1,0]
	v_pk_mul_f32 v[96:97], v[82:83], s[20:21] op_sel_hi:[1,0]
	v_pk_mul_f32 v[100:101], v[80:81], s[20:21] op_sel_hi:[1,0]
	v_pk_mul_f32 v[92:93], v[74:75], s[20:21] op_sel_hi:[1,0]
	v_pk_mul_f32 v[94:95], v[72:73], s[20:21] op_sel_hi:[1,0]
	v_pk_mul_f32 v[80:81], v[90:91], s[20:21] op_sel_hi:[1,0]
	v_pk_mul_f32 v[82:83], v[88:89], s[20:21] op_sel_hi:[1,0]
	v_pk_mul_f32 v[72:73], v[86:87], s[20:21] op_sel_hi:[1,0]
	v_pk_mul_f32 v[74:75], v[84:85], s[20:21] op_sel_hi:[1,0]
	v_pk_mul_f32 v[66:67], v[66:67], s[20:21] op_sel_hi:[1,0]
	v_pk_mul_f32 v[64:65], v[64:65], s[20:21] op_sel_hi:[1,0]
	v_pk_mul_f32 v[58:59], v[58:59], s[20:21] op_sel_hi:[1,0]
	v_pk_mul_f32 v[56:57], v[56:57], s[20:21] op_sel_hi:[1,0]
	v_pk_mul_f32 v[32:33], v[78:79], s[20:21] op_sel_hi:[1,0]
	v_pk_mul_f32 v[34:35], v[76:77], s[20:21] op_sel_hi:[1,0]
	v_pk_mul_f32 v[26:27], v[70:71], s[20:21] op_sel_hi:[1,0]
	v_pk_mul_f32 v[30:31], v[68:69], s[20:21] op_sel_hi:[1,0]
	v_pk_mul_f32 v[24:25], v[50:51], s[20:21] op_sel_hi:[1,0]
	v_pk_mul_f32 v[28:29], v[48:49], s[20:21] op_sel_hi:[1,0]
	v_pk_mul_f32 v[20:21], v[46:47], s[20:21] op_sel_hi:[1,0]
	v_pk_mul_f32 v[22:23], v[44:45], s[20:21] op_sel_hi:[1,0]
	v_pk_mul_f32 v[16:17], v[62:63], s[20:21] op_sel_hi:[1,0]
	v_pk_mul_f32 v[18:19], v[60:61], s[20:21] op_sel_hi:[1,0]
	v_pk_mul_f32 v[10:11], v[54:55], s[20:21] op_sel_hi:[1,0]
	v_pk_mul_f32 v[14:15], v[52:53], s[20:21] op_sel_hi:[1,0]
	v_pk_mul_f32 v[8:9], v[42:43], s[20:21] op_sel_hi:[1,0]
	v_pk_mul_f32 v[12:13], v[40:41], s[20:21] op_sel_hi:[1,0]
	v_pk_mul_f32 v[4:5], v[38:39], s[20:21] op_sel_hi:[1,0]
	v_pk_mul_f32 v[6:7], v[36:37], s[20:21] op_sel_hi:[1,0]
